# both gathers: each next-group v-row load issued right after the last use of its registers (not 16 at the tail); every expert's decode waits only for its own row with a counted vmcnt (checked by an in-
# speedup vs baseline: 1.0214x; 1.0013x over previous
.LBB0_763:
	s_cmpk_ge_i32 s58, 0x70
	s_cselect_b64 s[12:13], -1, 0
	ds_bpermute_b32 v84, v93, v92
	s_and_b64 vcc, s[12:13], s[48:49]
	v_cndmask_b32_e32 v104, v0, v94, vcc
	v_ashrrev_i32_e32 v105, 31, v104
	s_add_i32 s12, s58, 16
	s_and_b32 s12, s12, 0x70
	v_lshlrev_b64 v[104:105], 9, v[104:105]
	v_lshl_add_u64 v[104:105], s[94:95], 0, v[104:105]
	s_lshl_b32 s36, s12, 2
	s_waitcnt lgkmcnt(0)
	s_waitcnt vmcnt(32)
	v_mov_b32_e32 v92, v122
	v_ashrrev_i32_e32 v85, 31, v84
	v_lshl_add_u64 v[104:105], v[104:105], 0, s[36:37]
	v_lshl_add_u64 v[84:85], v[84:85], 3, s[8:9]
	v_lshl_add_u64 v[104:105], v[104:105], 0, v[144:145]
	global_load_dwordx2 v[84:85], v[84:85], off
	s_nop 0
	global_load_dword v86, v[72:73], off
	global_load_dword v122, v[104:105], off
	s_waitcnt vmcnt(19)
	v_dot8_i32_i4 v87, v8, v1, 0
	v_dot8_i32_i4 v104, v8, v88, 0
	v_dot8_i32_i4 v87, v9, v89, v87
	v_dot8_i32_i4 v104, v9, v90, v104
	s_waitcnt vmcnt(19)
	v_dot8_i32_i4 v9, v10, v88, 0
	v_dot8_i32_i4 v9, v11, v90, v9
	v_lshl_add_u32 v87, v87, 4, v104
	v_dot8_i32_i4 v8, v10, v1, 0
	v_dot8_i32_i4 v8, v11, v89, v8
	s_add_i32 s58, s58, 16
	v_lshl_add_u64 v[72:73], v[72:73], 0, 64
	s_nop 0
	v_lshl_add_u32 v104, v8, 4, v9
	v_dot8_i32_i4 v8, v12, v1, 0
	v_dot8_i32_i4 v9, v12, v88, 0
	v_dot8_i32_i4 v8, v13, v89, v8
	v_dot8_i32_i4 v9, v13, v90, v9
	v_readlane_b32 s12, v92, 0
	v_readlane_b32 s28, v92, 8
	v_readlane_b32 s30, v92, 9
	v_lshl_add_u32 v105, v8, 4, v9
	v_dot8_i32_i4 v8, v14, v1, 0
	v_dot8_i32_i4 v9, v14, v88, 0
	v_dot8_i32_i4 v8, v15, v89, v8
	v_dot8_i32_i4 v9, v15, v90, v9
	s_ashr_i32 s13, s12, 31
	v_readlane_b32 s14, v92, 1
	s_ashr_i32 s29, s28, 31
	v_lshl_add_u32 v106, v8, 4, v9
	v_dot8_i32_i4 v8, v16, v1, 0
	v_dot8_i32_i4 v9, v16, v88, 0
	v_dot8_i32_i4 v8, v17, v89, v8
	v_dot8_i32_i4 v9, v17, v90, v9
	s_ashr_i32 s31, s30, 31
	v_readlane_b32 s34, v92, 10
	s_lshl_b64 s[12:13], s[12:13], 9
	v_lshl_add_u32 v107, v8, 4, v9
	v_dot8_i32_i4 v8, v18, v1, 0
	v_dot8_i32_i4 v9, v18, v88, 0
	v_dot8_i32_i4 v8, v19, v89, v8
	v_dot8_i32_i4 v9, v19, v90, v9
	s_ashr_i32 s15, s14, 31
	v_readlane_b32 s16, v92, 2
	s_lshl_b64 s[28:29], s[28:29], 9
	v_lshl_add_u32 v108, v8, 4, v9
	v_dot8_i32_i4 v8, v20, v1, 0
	v_dot8_i32_i4 v9, v20, v88, 0
	v_dot8_i32_i4 v8, v21, v89, v8
	v_dot8_i32_i4 v9, v21, v90, v9
	s_lshl_b64 s[30:31], s[30:31], 9
	s_ashr_i32 s35, s34, 31
	v_readlane_b32 s38, v92, 11
	v_lshl_add_u32 v109, v8, 4, v9
	v_dot8_i32_i4 v8, v22, v1, 0
	v_dot8_i32_i4 v9, v22, v88, 0
	v_dot8_i32_i4 v8, v23, v89, v8
	v_dot8_i32_i4 v9, v23, v90, v9
	s_lshl_b64 s[14:15], s[14:15], 9
	s_ashr_i32 s17, s16, 31
	v_readlane_b32 s18, v92, 3
	v_lshl_add_u32 v110, v8, 4, v9
	v_dot8_i32_i4 v8, v24, v1, 0
	v_dot8_i32_i4 v9, v24, v88, 0
	v_dot8_i32_i4 v8, v25, v89, v8
	v_dot8_i32_i4 v9, v25, v90, v9
	s_lshl_b64 s[34:35], s[34:35], 9
	s_ashr_i32 s39, s38, 31
	s_nop 0
	v_lshl_add_u32 v111, v8, 4, v9
	v_dot8_i32_i4 v8, v38, v1, 0
	v_dot8_i32_i4 v9, v38, v88, 0
	v_dot8_i32_i4 v8, v39, v89, v8
	v_dot8_i32_i4 v9, v39, v90, v9
	s_setprio 2
	v_permlane32_swap_b32 v87, v111
	s_nop 1
	v_lshl_add_u32 v112, v8, 4, v9
	v_dot8_i32_i4 v8, v50, v1, 0
	v_dot8_i32_i4 v9, v50, v88, 0
	v_dot8_i32_i4 v8, v51, v89, v8
	v_dot8_i32_i4 v9, v51, v90, v9
	s_waitcnt lgkmcnt(0)
	v_add_u32_e32 v87, v87, v111
	v_permlane32_swap_b32 v104, v112
	v_lshl_add_u32 v113, v8, 4, v9
	v_dot8_i32_i4 v8, v48, v1, 0
	v_dot8_i32_i4 v9, v48, v88, 0
	v_dot8_i32_i4 v8, v49, v89, v8
	v_dot8_i32_i4 v9, v49, v90, v9
	s_waitcnt lgkmcnt(0)
	v_add_u32_e32 v104, v104, v112
	v_permlane32_swap_b32 v105, v113
	v_lshl_add_u32 v114, v8, 4, v9
	v_dot8_i32_i4 v8, v46, v1, 0
	v_dot8_i32_i4 v9, v46, v88, 0
	v_dot8_i32_i4 v8, v47, v89, v8
	v_dot8_i32_i4 v9, v47, v90, v9
	s_waitcnt lgkmcnt(0)
	v_add_u32_e32 v105, v105, v113
	v_permlane32_swap_b32 v106, v114
	v_lshl_add_u32 v115, v8, 4, v9
	v_dot8_i32_i4 v8, v44, v1, 0
	v_dot8_i32_i4 v9, v44, v88, 0
	v_dot8_i32_i4 v8, v45, v89, v8
	v_dot8_i32_i4 v9, v45, v90, v9
	s_waitcnt lgkmcnt(0)
	v_add_u32_e32 v106, v106, v114
	v_permlane32_swap_b32 v107, v115
	v_lshl_add_u32 v116, v8, 4, v9
	v_dot8_i32_i4 v8, v42, v1, 0
	v_dot8_i32_i4 v9, v42, v88, 0
	v_dot8_i32_i4 v8, v43, v89, v8
	v_dot8_i32_i4 v9, v43, v90, v9
	s_waitcnt lgkmcnt(0)
	v_add_u32_e32 v107, v107, v115
	v_permlane32_swap_b32 v108, v116
	v_lshl_add_u32 v117, v8, 4, v9
	v_dot8_i32_i4 v8, v40, v1, 0
	v_dot8_i32_i4 v9, v40, v88, 0
	v_dot8_i32_i4 v8, v41, v89, v8
	v_dot8_i32_i4 v9, v41, v90, v9
	s_waitcnt lgkmcnt(0)
	v_add_u32_e32 v108, v108, v116
	v_permlane32_swap_b32 v109, v117
	v_lshl_add_u32 v118, v8, 4, v9
	s_waitcnt lgkmcnt(0)
	v_add_u32_e32 v109, v109, v117
	v_permlane32_swap_b32 v110, v118
	v_readlane_b32 s50, v92, 12
	s_lshl_b64 s[16:17], s[16:17], 9
	s_ashr_i32 s19, s18, 31
	s_waitcnt lgkmcnt(0)
	v_add_u32_e32 v110, v110, v118
	v_permlane16_swap_b32 v87, v107
	v_readlane_b32 s20, v92, 4
	s_add_u32 s66, s28, s62
	s_addc_u32 s67, s29, s63
	global_load_dwordx2 v[24:25], v121, s[66:67]
	s_add_u32 s66, s30, s62
	s_addc_u32 s67, s31, s63
	global_load_dwordx2 v[38:39], v121, s[66:67]
	s_waitcnt lgkmcnt(0)
	v_add_u32_e32 v87, v87, v107
	v_permlane16_swap_b32 v104, v108
	s_lshl_b64 s[38:39], s[38:39], 9
	s_ashr_i32 s51, s50, 31
	v_readlane_b32 s52, v92, 13
	s_waitcnt lgkmcnt(0)
	v_add_u32_e32 v104, v104, v108
	v_permlane16_swap_b32 v105, v109
	s_lshl_b64 s[18:19], s[18:19], 9
	s_ashr_i32 s21, s20, 31
	v_readlane_b32 s22, v92, 5
	s_waitcnt lgkmcnt(0)
	v_add_u32_e32 v105, v105, v109
	v_permlane16_swap_b32 v106, v110
	s_add_u32 s66, s34, s62
	s_addc_u32 s67, s35, s63
	global_load_dwordx2 v[50:51], v121, s[66:67]
	s_lshl_b64 s[50:51], s[50:51], 9
	s_ashr_i32 s53, s52, 31
	s_waitcnt lgkmcnt(0)
	v_add_u32_e32 v106, v106, v110
	v_cndmask_b32_e64 v107, v87, v105, s[44:45]
	v_cndmask_b32_e64 v87, v105, v87, s[44:45]
	s_nop 0
	v_readlane_b32 s54, v92, 14
	s_lshl_b64 s[20:21], s[20:21], 9
	s_ashr_i32 s23, s22, 31
	v_readlane_b32 s24, v92, 6
	s_waitcnt lgkmcnt(0)
	v_add_u32_dpp v87, v107, v87 row_ror:8 row_mask:0xf bank_mask:0xf
	v_cndmask_b32_e64 v105, v104, v106, s[44:45]
	s_nop 1
	v_cndmask_b32_e64 v104, v106, v104, s[44:45]
	s_lshl_b64 s[52:53], s[52:53], 9
	s_ashr_i32 s55, s54, 31
	v_readlane_b32 s56, v92, 15
	s_waitcnt lgkmcnt(0)
	v_add_u32_dpp v104, v105, v104 row_ror:8 row_mask:0xf bank_mask:0xf
	v_cndmask_b32_e64 v105, v87, v104, s[46:47]
	v_cndmask_b32_e64 v87, v104, v87, s[46:47]
	s_nop 0
	v_mov_b32_dpp v104, v105 row_half_mirror row_mask:0xf bank_mask:0xf
	s_nop 1
	s_lshl_b64 s[22:23], s[22:23], 9
	s_ashr_i32 s25, s24, 31
	v_readlane_b32 s26, v92, 7
	s_lshl_b64 s[54:55], s[54:55], 9
	s_waitcnt lgkmcnt(0)
	v_add_u32_dpp v87, v104, v87 quad_perm:[3,2,1,0] row_mask:0xf bank_mask:0xf
	s_nop 1
	s_ashr_i32 s57, s56, 31
	s_lshl_b64 s[24:25], s[24:25], 9
	s_ashr_i32 s27, s26, 31
	s_lshl_b64 s[56:57], s[56:57], 9
	s_waitcnt lgkmcnt(0)
	v_add_u32_dpp v87, v87, v87 quad_perm:[2,3,0,1] row_mask:0xf bank_mask:0xf
	s_nop 1
	s_lshl_b64 s[26:27], s[26:27], 9
	s_add_u32 s66, s38, s62
	s_addc_u32 s67, s39, s63
	global_load_dwordx2 v[48:49], v121, s[66:67]
	s_add_u32 s66, s50, s62
	s_addc_u32 s67, s51, s63
	global_load_dwordx2 v[46:47], v121, s[66:67]
	s_add_u32 s66, s52, s62
	s_addc_u32 s67, s53, s63
	global_load_dwordx2 v[44:45], v121, s[66:67]
	s_add_u32 s66, s54, s62
	s_addc_u32 s67, s55, s63
	global_load_dwordx2 v[42:43], v121, s[66:67]
	s_add_u32 s66, s56, s62
	s_addc_u32 s67, s57, s63
	global_load_dwordx2 v[40:41], v121, s[66:67]
	s_add_u32 s66, s12, s62
	s_addc_u32 s67, s13, s63
	global_load_dwordx2 v[8:9], v121, s[66:67]
	s_add_u32 s66, s14, s62
	s_addc_u32 s67, s15, s63
	global_load_dwordx2 v[10:11], v121, s[66:67]
	s_add_u32 s66, s16, s62
	s_addc_u32 s67, s17, s63
	global_load_dwordx2 v[12:13], v121, s[66:67]
	s_add_u32 s66, s18, s62
	s_addc_u32 s67, s19, s63
	global_load_dwordx2 v[14:15], v121, s[66:67]
	s_add_u32 s66, s20, s62
	s_addc_u32 s67, s21, s63
	global_load_dwordx2 v[16:17], v121, s[66:67]
	s_add_u32 s66, s22, s62
	s_addc_u32 s67, s23, s63
	global_load_dwordx2 v[18:19], v121, s[66:67]
	s_add_u32 s66, s24, s62
	s_addc_u32 s67, s25, s63
	global_load_dwordx2 v[20:21], v121, s[66:67]
	s_add_u32 s66, s26, s62
	s_addc_u32 s67, s27, s63
	global_load_dwordx2 v[22:23], v121, s[66:67]
	s_waitcnt lgkmcnt(0)
	v_add_u32_dpp v87, v87, v87 quad_perm:[1,0,3,2] row_mask:0xf bank_mask:0xf
	s_waitcnt vmcnt(17)
	v_mul_f32_e32 v85, v91, v85
	v_cvt_f32_i32_e32 v87, v87
	v_add_f32_e32 v87, v95, v87
	v_mul_f32_e32 v85, v85, v87
	v_mul_f32_e32 v87, 0x3d372713, v85
	v_mul_f32_e32 v87, v85, v87
	v_fma_f32 v87, v85, v87, v85
	v_mul_f32_e32 v87, 0x3fcc422a, v87
	v_mul_f32_e32 v87, 0xbfb8aa3b, v87
	v_exp_f32_e32 v87, v87
	s_nop 0
	v_add_f32_e32 v87, 1.0, v87
	v_rcp_f32_e32 v87, v87
	s_nop 0
	v_pk_mul_f32 v[84:85], v[84:85], v[86:87]
	s_waitcnt vmcnt(34)
	v_alignbit_b32 v224, v82, v82, 4
	v_pk_mul_f32 v[84:85], v[84:85], v[84:85] op_sel:[0,1] op_sel_hi:[1,0]
	v_cvt_f16_f32_e32 v120, v84
	s_setprio 0
	v_and_b32_e32 v86, 0x7070707, v82
	v_readlane_b32 s36, v120, 0
	v_and_b32_e32 v87, 0x7070707, v224
	v_perm_b32 v86, s2, v205, v86
	v_perm_b32 v87, s2, v205, v87
	v_and_or_b32 v86, v82, s4, v86
	v_and_or_b32 v82, v224, s4, v87
	v_perm_b32 v87, v82, v86, s5
	v_perm_b32 v104, v82, v86, s33
	v_perm_b32 v105, v82, v86, s0
	v_perm_b32 v82, v82, v86, s1
	v_pk_fma_f16 v86, v87, s36, v103 op_sel_hi:[1,0,1]
	v_pk_fma_f16 v87, v104, s36, v102 op_sel_hi:[1,0,1]
	v_alignbit_b32 v225, v83, v83, 4
	v_pk_fma_f16 v82, v82, s36, v100 op_sel_hi:[1,0,1]
	v_and_b32_e32 v100, 0x7070707, v83
	v_and_b32_e32 v102, 0x7070707, v225
	v_perm_b32 v100, s2, v205, v100
	v_perm_b32 v102, s2, v205, v102
	v_and_or_b32 v100, v83, s4, v100
	v_and_or_b32 v83, v225, s4, v102
	v_perm_b32 v102, v83, v100, s5
	v_perm_b32 v103, v83, v100, s33
	v_perm_b32 v104, v83, v100, s0
	v_perm_b32 v83, v83, v100, s1
	v_readlane_b32 s59, v120, 4
	s_waitcnt vmcnt(33)
	v_alignbit_b32 v224, v80, v80, 4
	v_pk_fma_f16 v101, v105, s36, v101 op_sel_hi:[1,0,1]
	v_pk_fma_f16 v99, v102, s36, v99 op_sel_hi:[1,0,1]
	v_pk_fma_f16 v98, v103, s36, v98 op_sel_hi:[1,0,1]
	v_pk_fma_f16 v97, v104, s36, v97 op_sel_hi:[1,0,1]
	v_pk_fma_f16 v83, v83, s36, v96 op_sel_hi:[1,0,1]
	v_and_b32_e32 v96, 0x7070707, v80
	v_and_b32_e32 v100, 0x7070707, v224
	v_perm_b32 v96, s2, v205, v96
	v_perm_b32 v100, s2, v205, v100
	v_and_or_b32 v96, v80, s4, v96
	v_and_or_b32 v80, v224, s4, v100
	v_perm_b32 v100, v80, v96, s5
	v_perm_b32 v102, v80, v96, s33
	v_perm_b32 v103, v80, v96, s0
	v_perm_b32 v80, v80, v96, s1
	v_pk_fma_f16 v86, v100, s59, v86 op_sel_hi:[1,0,1]
	v_alignbit_b32 v225, v81, v81, 4
	v_pk_fma_f16 v80, v80, s59, v82 op_sel_hi:[1,0,1]
	v_and_b32_e32 v82, 0x7070707, v81
	v_and_b32_e32 v100, 0x7070707, v225
	v_pk_fma_f16 v96, v103, s59, v101 op_sel_hi:[1,0,1]
	v_perm_b32 v82, s2, v205, v82
	v_perm_b32 v100, s2, v205, v100
	v_and_or_b32 v82, v81, s4, v82
	v_and_or_b32 v81, v225, s4, v100
	v_perm_b32 v100, v81, v82, s5
	v_pk_fma_f16 v87, v102, s59, v87 op_sel_hi:[1,0,1]
	v_perm_b32 v101, v81, v82, s33
	v_perm_b32 v102, v81, v82, s0
	v_perm_b32 v81, v81, v82, s1
	v_pk_fma_f16 v82, v100, s59, v99 op_sel_hi:[1,0,1]
	v_readlane_b32 s60, v120, 8
	s_waitcnt vmcnt(32)
	v_alignbit_b32 v224, v78, v78, 4
	v_pk_fma_f16 v98, v101, s59, v98 op_sel_hi:[1,0,1]
	v_pk_fma_f16 v97, v102, s59, v97 op_sel_hi:[1,0,1]
	v_pk_fma_f16 v81, v81, s59, v83 op_sel_hi:[1,0,1]
	v_and_b32_e32 v85, 0x7070707, v78
	v_and_b32_e32 v99, 0x7070707, v224
	v_perm_b32 v85, s2, v205, v85
	v_perm_b32 v99, s2, v205, v99
	v_and_or_b32 v85, v78, s4, v85
	v_and_or_b32 v78, v224, s4, v99
	v_perm_b32 v99, v78, v85, s5
	v_perm_b32 v100, v78, v85, s33
	v_perm_b32 v101, v78, v85, s0
	v_perm_b32 v78, v78, v85, s1
	v_pk_fma_f16 v85, v99, s60, v86 op_sel_hi:[1,0,1]
	v_pk_fma_f16 v86, v100, s60, v87 op_sel_hi:[1,0,1]
	v_pk_fma_f16 v87, v101, s60, v96 op_sel_hi:[1,0,1]
	v_alignbit_b32 v225, v79, v79, 4
	v_pk_fma_f16 v78, v78, s60, v80 op_sel_hi:[1,0,1]
	v_and_b32_e32 v80, 0x7070707, v79
	v_and_b32_e32 v96, 0x7070707, v225
	v_perm_b32 v80, s2, v205, v80
	v_perm_b32 v96, s2, v205, v96
	v_and_or_b32 v80, v79, s4, v80
	v_and_or_b32 v79, v225, s4, v96
	v_perm_b32 v96, v79, v80, s5
	v_perm_b32 v100, v79, v80, s0
	v_perm_b32 v99, v79, v80, s33
	v_perm_b32 v79, v79, v80, s1
	v_pk_fma_f16 v80, v96, s60, v82 op_sel_hi:[1,0,1]
	v_pk_fma_f16 v96, v100, s60, v97 op_sel_hi:[1,0,1]
	v_readlane_b32 s36, v120, 12
	s_waitcnt vmcnt(31)
	v_alignbit_b32 v224, v76, v76, 4
	v_pk_fma_f16 v82, v99, s60, v98 op_sel_hi:[1,0,1]
	v_pk_fma_f16 v79, v79, s60, v81 op_sel_hi:[1,0,1]
	v_and_b32_e32 v83, 0x7070707, v76
	v_and_b32_e32 v97, 0x7070707, v224
	v_perm_b32 v83, s2, v205, v83
	v_perm_b32 v97, s2, v205, v97
	v_and_or_b32 v83, v76, s4, v83
	v_and_or_b32 v76, v224, s4, v97
	v_perm_b32 v97, v76, v83, s5
	v_perm_b32 v98, v76, v83, s33
	v_perm_b32 v99, v76, v83, s0
	v_perm_b32 v76, v76, v83, s1
	v_pk_fma_f16 v83, v97, s36, v85 op_sel_hi:[1,0,1]
	v_pk_fma_f16 v85, v98, s36, v86 op_sel_hi:[1,0,1]
	v_pk_fma_f16 v86, v99, s36, v87 op_sel_hi:[1,0,1]
	v_alignbit_b32 v225, v77, v77, 4
	v_pk_fma_f16 v76, v76, s36, v78 op_sel_hi:[1,0,1]
	v_and_b32_e32 v78, 0x7070707, v77
	v_and_b32_e32 v87, 0x7070707, v225
	v_perm_b32 v78, s2, v205, v78
	v_perm_b32 v87, s2, v205, v87
	v_and_or_b32 v78, v77, s4, v78
	v_and_or_b32 v77, v225, s4, v87
	v_perm_b32 v87, v77, v78, s5
	v_perm_b32 v97, v77, v78, s33
	v_perm_b32 v98, v77, v78, s0
	v_perm_b32 v77, v77, v78, s1
	v_pk_fma_f16 v78, v87, s36, v80 op_sel_hi:[1,0,1]
	v_readlane_b32 s59, v120, 16
	s_waitcnt vmcnt(30)
	v_alignbit_b32 v224, v74, v74, 4
	v_pk_fma_f16 v80, v97, s36, v82 op_sel_hi:[1,0,1]
	v_pk_fma_f16 v82, v98, s36, v96 op_sel_hi:[1,0,1]
	v_pk_fma_f16 v77, v77, s36, v79 op_sel_hi:[1,0,1]
	v_and_b32_e32 v81, 0x7070707, v74
	v_and_b32_e32 v87, 0x7070707, v224
	v_perm_b32 v81, s2, v205, v81
	v_perm_b32 v87, s2, v205, v87
	v_and_or_b32 v81, v74, s4, v81
	v_and_or_b32 v74, v224, s4, v87
	v_perm_b32 v87, v74, v81, s5
	v_perm_b32 v96, v74, v81, s33
	v_perm_b32 v97, v74, v81, s0
	v_perm_b32 v74, v74, v81, s1
	v_pk_fma_f16 v81, v87, s59, v83 op_sel_hi:[1,0,1]
	v_pk_fma_f16 v83, v96, s59, v85 op_sel_hi:[1,0,1]
	v_pk_fma_f16 v85, v97, s59, v86 op_sel_hi:[1,0,1]
	v_alignbit_b32 v225, v75, v75, 4
	v_pk_fma_f16 v74, v74, s59, v76 op_sel_hi:[1,0,1]
	v_and_b32_e32 v76, 0x7070707, v75
	v_and_b32_e32 v86, 0x7070707, v225
	v_perm_b32 v76, s2, v205, v76
	v_perm_b32 v86, s2, v205, v86
	v_and_or_b32 v76, v75, s4, v76
	v_and_or_b32 v75, v225, s4, v86
	v_perm_b32 v86, v75, v76, s5
	v_perm_b32 v87, v75, v76, s33
	v_perm_b32 v96, v75, v76, s0
	v_perm_b32 v75, v75, v76, s1
	v_pk_fma_f16 v76, v86, s59, v78 op_sel_hi:[1,0,1]
	v_pk_fma_f16 v78, v87, s59, v80 op_sel_hi:[1,0,1]
	v_pk_fma_f16 v80, v96, s59, v82 op_sel_hi:[1,0,1]
	v_readlane_b32 s60, v120, 20
	s_waitcnt vmcnt(29)
	v_alignbit_b32 v224, v70, v70, 4
	v_pk_fma_f16 v75, v75, s59, v77 op_sel_hi:[1,0,1]
	v_and_b32_e32 v79, 0x7070707, v70
	v_and_b32_e32 v82, 0x7070707, v224
	v_perm_b32 v79, s2, v205, v79
	v_perm_b32 v82, s2, v205, v82
	v_and_or_b32 v79, v70, s4, v79
	v_and_or_b32 v70, v224, s4, v82
	v_perm_b32 v82, v70, v79, s5
	v_perm_b32 v86, v70, v79, s33
	v_perm_b32 v87, v70, v79, s0
	v_perm_b32 v70, v70, v79, s1
	v_pk_fma_f16 v79, v82, s60, v81 op_sel_hi:[1,0,1]
	v_pk_fma_f16 v81, v86, s60, v83 op_sel_hi:[1,0,1]
	v_alignbit_b32 v225, v71, v71, 4
	v_pk_fma_f16 v70, v70, s60, v74 op_sel_hi:[1,0,1]
	v_and_b32_e32 v74, 0x7070707, v71
	v_and_b32_e32 v83, 0x7070707, v225
	v_pk_fma_f16 v82, v87, s60, v85 op_sel_hi:[1,0,1]
	v_perm_b32 v74, s2, v205, v74
	v_perm_b32 v83, s2, v205, v83
	v_and_or_b32 v74, v71, s4, v74
	v_and_or_b32 v71, v225, s4, v83
	v_perm_b32 v83, v71, v74, s5
	v_perm_b32 v85, v71, v74, s33
	v_perm_b32 v86, v71, v74, s0
	v_perm_b32 v71, v71, v74, s1
	v_pk_fma_f16 v74, v83, s60, v76 op_sel_hi:[1,0,1]
	v_pk_fma_f16 v76, v85, s60, v78 op_sel_hi:[1,0,1]
	v_pk_fma_f16 v78, v86, s60, v80 op_sel_hi:[1,0,1]
	v_readlane_b32 s36, v120, 24
	s_waitcnt vmcnt(28)
	v_alignbit_b32 v224, v68, v68, 4
	v_pk_fma_f16 v71, v71, s60, v75 op_sel_hi:[1,0,1]
	v_and_b32_e32 v77, 0x7070707, v68
	v_and_b32_e32 v80, 0x7070707, v224
	v_perm_b32 v77, s2, v205, v77
	v_perm_b32 v80, s2, v205, v80
	v_and_or_b32 v77, v68, s4, v77
	v_and_or_b32 v68, v224, s4, v80
	v_perm_b32 v80, v68, v77, s5
	v_perm_b32 v83, v68, v77, s33
	v_perm_b32 v85, v68, v77, s0
	v_perm_b32 v68, v68, v77, s1
	v_pk_fma_f16 v77, v80, s36, v79 op_sel_hi:[1,0,1]
	v_pk_fma_f16 v79, v83, s36, v81 op_sel_hi:[1,0,1]
	v_alignbit_b32 v225, v69, v69, 4
	v_pk_fma_f16 v68, v68, s36, v70 op_sel_hi:[1,0,1]
	v_and_b32_e32 v70, 0x7070707, v69
	v_and_b32_e32 v81, 0x7070707, v225
	v_pk_fma_f16 v80, v85, s36, v82 op_sel_hi:[1,0,1]
	v_perm_b32 v70, s2, v205, v70
	v_perm_b32 v81, s2, v205, v81
	v_and_or_b32 v70, v69, s4, v70
	v_and_or_b32 v69, v225, s4, v81
	v_perm_b32 v81, v69, v70, s5
	v_perm_b32 v82, v69, v70, s33
	v_perm_b32 v83, v69, v70, s0
	v_perm_b32 v69, v69, v70, s1
	v_pk_fma_f16 v70, v81, s36, v74 op_sel_hi:[1,0,1]
	v_pk_fma_f16 v74, v82, s36, v76 op_sel_hi:[1,0,1]
	v_pk_fma_f16 v76, v83, s36, v78 op_sel_hi:[1,0,1]
	v_readlane_b32 s59, v120, 28
	s_waitcnt vmcnt(25)
	v_alignbit_b32 v224, v64, v64, 4
	v_pk_fma_f16 v69, v69, s36, v71 op_sel_hi:[1,0,1]
	v_and_b32_e32 v75, 0x7070707, v64
	v_and_b32_e32 v78, 0x7070707, v224
	v_perm_b32 v75, s2, v205, v75
	v_perm_b32 v78, s2, v205, v78
	v_and_or_b32 v75, v64, s4, v75
	v_and_or_b32 v64, v224, s4, v78
	v_perm_b32 v78, v64, v75, s5
	v_perm_b32 v81, v64, v75, s33
	v_perm_b32 v82, v64, v75, s0
	v_perm_b32 v64, v64, v75, s1
	v_pk_fma_f16 v75, v78, s59, v77 op_sel_hi:[1,0,1]
	v_pk_fma_f16 v77, v81, s59, v79 op_sel_hi:[1,0,1]
	v_alignbit_b32 v225, v65, v65, 4
	v_pk_fma_f16 v64, v64, s59, v68 op_sel_hi:[1,0,1]
	v_and_b32_e32 v68, 0x7070707, v65
	v_and_b32_e32 v79, 0x7070707, v225
	v_pk_fma_f16 v78, v82, s59, v80 op_sel_hi:[1,0,1]
	s_add_u32 s66, s12, s64
	s_addc_u32 s67, s13, s65
	global_load_dwordx2 v[82:83], v121, s[66:67]
	v_perm_b32 v68, s2, v205, v68
	v_perm_b32 v79, s2, v205, v79
	v_and_or_b32 v68, v65, s4, v68
	v_and_or_b32 v65, v225, s4, v79
	v_perm_b32 v79, v65, v68, s5
	v_perm_b32 v80, v65, v68, s33
	v_perm_b32 v81, v65, v68, s0
	v_perm_b32 v65, v65, v68, s1
	v_pk_fma_f16 v68, v79, s59, v70 op_sel_hi:[1,0,1]
	v_pk_fma_f16 v70, v80, s59, v74 op_sel_hi:[1,0,1]
	v_pk_fma_f16 v74, v81, s59, v76 op_sel_hi:[1,0,1]
	v_readlane_b32 s60, v120, 32
	s_waitcnt vmcnt(25)
	v_alignbit_b32 v224, v62, v62, 4
	v_pk_fma_f16 v65, v65, s59, v69 op_sel_hi:[1,0,1]
	v_and_b32_e32 v71, 0x7070707, v62
	v_and_b32_e32 v76, 0x7070707, v224
	v_perm_b32 v71, s2, v205, v71
	v_perm_b32 v76, s2, v205, v76
	v_and_or_b32 v71, v62, s4, v71
	v_and_or_b32 v62, v224, s4, v76
	v_perm_b32 v76, v62, v71, s5
	v_perm_b32 v79, v62, v71, s33
	v_perm_b32 v80, v62, v71, s0
	v_perm_b32 v62, v62, v71, s1
	v_pk_fma_f16 v71, v76, s60, v75 op_sel_hi:[1,0,1]
	v_pk_fma_f16 v75, v79, s60, v77 op_sel_hi:[1,0,1]
	v_alignbit_b32 v225, v63, v63, 4
	v_pk_fma_f16 v62, v62, s60, v64 op_sel_hi:[1,0,1]
	v_and_b32_e32 v64, 0x7070707, v63
	v_and_b32_e32 v77, 0x7070707, v225
	v_pk_fma_f16 v76, v80, s60, v78 op_sel_hi:[1,0,1]
	s_add_u32 s66, s14, s64
	s_addc_u32 s67, s15, s65
	global_load_dwordx2 v[80:81], v121, s[66:67]
	v_perm_b32 v64, s2, v205, v64
	v_perm_b32 v77, s2, v205, v77
	v_and_or_b32 v64, v63, s4, v64
	v_and_or_b32 v63, v225, s4, v77
	v_perm_b32 v77, v63, v64, s5
	v_perm_b32 v78, v63, v64, s33
	v_perm_b32 v79, v63, v64, s0
	v_perm_b32 v63, v63, v64, s1
	v_pk_fma_f16 v64, v77, s60, v68 op_sel_hi:[1,0,1]
	v_pk_fma_f16 v68, v78, s60, v70 op_sel_hi:[1,0,1]
	v_pk_fma_f16 v70, v79, s60, v74 op_sel_hi:[1,0,1]
	v_readlane_b32 s36, v120, 36
	s_waitcnt vmcnt(29)
	v_alignbit_b32 v224, v66, v66, 4
	v_pk_fma_f16 v63, v63, s60, v65 op_sel_hi:[1,0,1]
	v_and_b32_e32 v69, 0x7070707, v66
	v_and_b32_e32 v74, 0x7070707, v224
	v_perm_b32 v69, s2, v205, v69
	v_perm_b32 v74, s2, v205, v74
	v_and_or_b32 v69, v66, s4, v69
	v_and_or_b32 v66, v224, s4, v74
	v_perm_b32 v74, v66, v69, s5
	v_perm_b32 v77, v66, v69, s33
	v_perm_b32 v78, v66, v69, s0
	v_perm_b32 v66, v66, v69, s1
	v_pk_fma_f16 v69, v74, s36, v71 op_sel_hi:[1,0,1]
	v_pk_fma_f16 v71, v77, s36, v75 op_sel_hi:[1,0,1]
	v_alignbit_b32 v225, v67, v67, 4
	v_pk_fma_f16 v62, v66, s36, v62 op_sel_hi:[1,0,1]
	v_and_b32_e32 v66, 0x7070707, v67
	v_and_b32_e32 v75, 0x7070707, v225
	v_pk_fma_f16 v74, v78, s36, v76 op_sel_hi:[1,0,1]
	s_add_u32 s66, s16, s64
	s_addc_u32 s67, s17, s65
	global_load_dwordx2 v[78:79], v121, s[66:67]
	v_perm_b32 v66, s2, v205, v66
	v_perm_b32 v75, s2, v205, v75
	v_and_or_b32 v66, v67, s4, v66
	v_and_or_b32 v67, v225, s4, v75
	v_perm_b32 v76, v67, v66, s33
	v_perm_b32 v77, v67, v66, s0
	v_perm_b32 v75, v67, v66, s5
	v_perm_b32 v66, v67, v66, s1
	v_pk_fma_f16 v67, v76, s36, v68 op_sel_hi:[1,0,1]
	v_pk_fma_f16 v68, v77, s36, v70 op_sel_hi:[1,0,1]
	v_readlane_b32 s59, v120, 40
	s_waitcnt vmcnt(26)
	v_alignbit_b32 v224, v60, v60, 4
	v_pk_fma_f16 v64, v75, s36, v64 op_sel_hi:[1,0,1]
	v_pk_fma_f16 v63, v66, s36, v63 op_sel_hi:[1,0,1]
	v_and_b32_e32 v66, 0x7070707, v60
	v_and_b32_e32 v70, 0x7070707, v224
	v_perm_b32 v66, s2, v205, v66
	v_perm_b32 v70, s2, v205, v70
	v_and_or_b32 v66, v60, s4, v66
	v_and_or_b32 v60, v224, s4, v70
	v_perm_b32 v70, v60, v66, s5
	v_perm_b32 v75, v60, v66, s33
	v_perm_b32 v76, v60, v66, s0
	v_perm_b32 v60, v60, v66, s1
	v_pk_fma_f16 v66, v70, s59, v69 op_sel_hi:[1,0,1]
	v_pk_fma_f16 v69, v75, s59, v71 op_sel_hi:[1,0,1]
	v_alignbit_b32 v225, v61, v61, 4
	v_pk_fma_f16 v60, v60, s59, v62 op_sel_hi:[1,0,1]
	v_and_b32_e32 v62, 0x7070707, v61
	v_and_b32_e32 v71, 0x7070707, v225
	v_pk_fma_f16 v70, v76, s59, v74 op_sel_hi:[1,0,1]
	s_add_u32 s66, s18, s64
	s_addc_u32 s67, s19, s65
	global_load_dwordx2 v[76:77], v121, s[66:67]
	v_perm_b32 v62, s2, v205, v62
	v_perm_b32 v71, s2, v205, v71
	v_and_or_b32 v62, v61, s4, v62
	v_and_or_b32 v61, v225, s4, v71
	v_perm_b32 v71, v61, v62, s5
	v_perm_b32 v74, v61, v62, s33
	v_perm_b32 v75, v61, v62, s0
	v_perm_b32 v61, v61, v62, s1
	v_pk_fma_f16 v62, v71, s59, v64 op_sel_hi:[1,0,1]
	v_pk_fma_f16 v64, v74, s59, v67 op_sel_hi:[1,0,1]
	v_pk_fma_f16 v67, v75, s59, v68 op_sel_hi:[1,0,1]
	v_readlane_b32 s60, v120, 44
	s_waitcnt vmcnt(26)
	v_alignbit_b32 v224, v58, v58, 4
	v_pk_fma_f16 v61, v61, s59, v63 op_sel_hi:[1,0,1]
	v_and_b32_e32 v65, 0x7070707, v58
	v_and_b32_e32 v68, 0x7070707, v224
	v_perm_b32 v65, s2, v205, v65
	v_perm_b32 v68, s2, v205, v68
	v_and_or_b32 v65, v58, s4, v65
	v_and_or_b32 v58, v224, s4, v68
	v_perm_b32 v68, v58, v65, s5
	v_perm_b32 v71, v58, v65, s33
	v_perm_b32 v74, v58, v65, s0
	v_perm_b32 v58, v58, v65, s1
	v_pk_fma_f16 v65, v68, s60, v66 op_sel_hi:[1,0,1]
	v_pk_fma_f16 v66, v71, s60, v69 op_sel_hi:[1,0,1]
	v_alignbit_b32 v225, v59, v59, 4
	v_pk_fma_f16 v58, v58, s60, v60 op_sel_hi:[1,0,1]
	v_and_b32_e32 v60, 0x7070707, v59
	v_and_b32_e32 v69, 0x7070707, v225
	v_pk_fma_f16 v68, v74, s60, v70 op_sel_hi:[1,0,1]
	s_add_u32 s66, s20, s64
	s_addc_u32 s67, s21, s65
	global_load_dwordx2 v[74:75], v121, s[66:67]
	v_perm_b32 v60, s2, v205, v60
	v_perm_b32 v69, s2, v205, v69
	v_and_or_b32 v60, v59, s4, v60
	v_and_or_b32 v59, v225, s4, v69
	v_perm_b32 v69, v59, v60, s5
	v_perm_b32 v70, v59, v60, s33
	v_perm_b32 v71, v59, v60, s0
	v_perm_b32 v59, v59, v60, s1
	v_pk_fma_f16 v60, v69, s60, v62 op_sel_hi:[1,0,1]
	v_pk_fma_f16 v62, v70, s60, v64 op_sel_hi:[1,0,1]
	v_pk_fma_f16 v64, v71, s60, v67 op_sel_hi:[1,0,1]
	v_readlane_b32 s36, v120, 48
	s_waitcnt vmcnt(26)
	v_alignbit_b32 v224, v56, v56, 4
	v_pk_fma_f16 v59, v59, s60, v61 op_sel_hi:[1,0,1]
	v_and_b32_e32 v63, 0x7070707, v56
	v_and_b32_e32 v67, 0x7070707, v224
	v_perm_b32 v63, s2, v205, v63
	v_perm_b32 v67, s2, v205, v67
	v_and_or_b32 v63, v56, s4, v63
	v_and_or_b32 v56, v224, s4, v67
	v_perm_b32 v67, v56, v63, s5
	v_perm_b32 v69, v56, v63, s33
	v_perm_b32 v70, v56, v63, s0
	v_perm_b32 v56, v56, v63, s1
	v_pk_fma_f16 v63, v67, s36, v65 op_sel_hi:[1,0,1]
	v_alignbit_b32 v225, v57, v57, 4
	v_pk_fma_f16 v56, v56, s36, v58 op_sel_hi:[1,0,1]
	v_and_b32_e32 v58, 0x7070707, v57
	v_and_b32_e32 v67, 0x7070707, v225
	v_pk_fma_f16 v65, v69, s36, v66 op_sel_hi:[1,0,1]
	v_pk_fma_f16 v66, v70, s36, v68 op_sel_hi:[1,0,1]
	s_add_u32 s66, s22, s64
	s_addc_u32 s67, s23, s65
	global_load_dwordx2 v[70:71], v121, s[66:67]
	v_perm_b32 v58, s2, v205, v58
	v_perm_b32 v67, s2, v205, v67
	v_and_or_b32 v58, v57, s4, v58
	v_and_or_b32 v57, v225, s4, v67
	v_perm_b32 v67, v57, v58, s5
	v_perm_b32 v68, v57, v58, s33
	v_perm_b32 v69, v57, v58, s0
	v_perm_b32 v57, v57, v58, s1
	v_pk_fma_f16 v58, v67, s36, v60 op_sel_hi:[1,0,1]
	v_pk_fma_f16 v60, v68, s36, v62 op_sel_hi:[1,0,1]
	v_pk_fma_f16 v62, v69, s36, v64 op_sel_hi:[1,0,1]
	v_readlane_b32 s59, v120, 52
	s_waitcnt vmcnt(26)
	v_alignbit_b32 v224, v54, v54, 4
	v_pk_fma_f16 v57, v57, s36, v59 op_sel_hi:[1,0,1]
	v_and_b32_e32 v61, 0x7070707, v54
	v_and_b32_e32 v64, 0x7070707, v224
	v_perm_b32 v61, s2, v205, v61
	v_perm_b32 v64, s2, v205, v64
	v_and_or_b32 v61, v54, s4, v61
	v_and_or_b32 v54, v224, s4, v64
	v_perm_b32 v64, v54, v61, s5
	v_perm_b32 v67, v54, v61, s33
	v_perm_b32 v68, v54, v61, s0
	v_perm_b32 v54, v54, v61, s1
	v_pk_fma_f16 v61, v64, s59, v63 op_sel_hi:[1,0,1]
	v_pk_fma_f16 v63, v67, s59, v65 op_sel_hi:[1,0,1]
	v_alignbit_b32 v225, v55, v55, 4
	v_pk_fma_f16 v54, v54, s59, v56 op_sel_hi:[1,0,1]
	v_and_b32_e32 v56, 0x7070707, v55
	v_and_b32_e32 v65, 0x7070707, v225
	v_pk_fma_f16 v64, v68, s59, v66 op_sel_hi:[1,0,1]
	s_add_u32 s66, s24, s64
	s_addc_u32 s67, s25, s65
	global_load_dwordx2 v[68:69], v121, s[66:67]
	v_perm_b32 v56, s2, v205, v56
	v_perm_b32 v65, s2, v205, v65
	v_and_or_b32 v56, v55, s4, v56
	v_and_or_b32 v55, v225, s4, v65
	v_perm_b32 v65, v55, v56, s5
	v_perm_b32 v66, v55, v56, s33
	v_perm_b32 v67, v55, v56, s0
	v_perm_b32 v55, v55, v56, s1
	v_pk_fma_f16 v56, v65, s59, v58 op_sel_hi:[1,0,1]
	v_pk_fma_f16 v58, v66, s59, v60 op_sel_hi:[1,0,1]
	v_pk_fma_f16 v60, v67, s59, v62 op_sel_hi:[1,0,1]
	v_readlane_b32 s60, v120, 56
	s_waitcnt vmcnt(26)
	v_alignbit_b32 v224, v52, v52, 4
	v_pk_fma_f16 v55, v55, s59, v57 op_sel_hi:[1,0,1]
	v_and_b32_e32 v59, 0x7070707, v52
	v_and_b32_e32 v62, 0x7070707, v224
	v_perm_b32 v59, s2, v205, v59
	v_perm_b32 v62, s2, v205, v62
	v_and_or_b32 v59, v52, s4, v59
	v_and_or_b32 v52, v224, s4, v62
	v_perm_b32 v62, v52, v59, s5
	v_perm_b32 v65, v52, v59, s33
	v_perm_b32 v66, v52, v59, s0
	v_perm_b32 v52, v52, v59, s1
	v_pk_fma_f16 v59, v62, s60, v61 op_sel_hi:[1,0,1]
	v_pk_fma_f16 v61, v65, s60, v63 op_sel_hi:[1,0,1]
	v_alignbit_b32 v225, v53, v53, 4
	v_pk_fma_f16 v52, v52, s60, v54 op_sel_hi:[1,0,1]
	v_and_b32_e32 v54, 0x7070707, v53
	v_and_b32_e32 v63, 0x7070707, v225
	v_pk_fma_f16 v62, v66, s60, v64 op_sel_hi:[1,0,1]
	s_add_u32 s66, s30, s64
	s_addc_u32 s67, s31, s65
	global_load_dwordx2 v[66:67], v121, s[66:67]
	v_perm_b32 v54, s2, v205, v54
	v_perm_b32 v63, s2, v205, v63
	v_and_or_b32 v54, v53, s4, v54
	v_and_or_b32 v53, v225, s4, v63
	v_perm_b32 v63, v53, v54, s5
	v_perm_b32 v64, v53, v54, s33
	v_perm_b32 v65, v53, v54, s0
	v_perm_b32 v53, v53, v54, s1
	v_pk_fma_f16 v54, v63, s60, v56 op_sel_hi:[1,0,1]
	v_pk_fma_f16 v56, v64, s60, v58 op_sel_hi:[1,0,1]
	v_pk_fma_f16 v58, v65, s60, v60 op_sel_hi:[1,0,1]
	v_readlane_b32 s36, v120, 60
	s_waitcnt vmcnt(34)
	v_alignbit_b32 v224, v36, v36, 4
	v_pk_fma_f16 v53, v53, s60, v55 op_sel_hi:[1,0,1]
	v_and_b32_e32 v57, 0x7070707, v36
	v_and_b32_e32 v60, 0x7070707, v224
	v_perm_b32 v57, s2, v205, v57
	v_perm_b32 v60, s2, v205, v60
	v_and_or_b32 v57, v36, s4, v57
	v_and_or_b32 v36, v224, s4, v60
	v_perm_b32 v60, v36, v57, s5
	v_perm_b32 v63, v36, v57, s33
	v_perm_b32 v64, v36, v57, s0
	v_perm_b32 v36, v36, v57, s1
	v_pk_fma_f16 v100, v36, s36, v52 op_sel_hi:[1,0,1]
	v_alignbit_b32 v225, v37, v37, 4
	v_and_b32_e32 v36, 0x7070707, v37
	v_and_b32_e32 v52, 0x7070707, v225
	v_perm_b32 v36, s2, v205, v36
	v_perm_b32 v52, s2, v205, v52
	v_and_or_b32 v36, v37, s4, v36
	v_and_or_b32 v37, v225, s4, v52
	v_pk_fma_f16 v103, v60, s36, v59 op_sel_hi:[1,0,1]
	v_perm_b32 v52, v37, v36, s5
	v_perm_b32 v57, v37, v36, s33
	v_perm_b32 v59, v37, v36, s0
	v_perm_b32 v36, v37, v36, s1
	v_pk_fma_f16 v96, v36, s36, v53 op_sel_hi:[1,0,1]
	s_add_u32 s66, s56, s64
	s_addc_u32 s67, s57, s65
	global_load_dwordx2 v[36:37], v121, s[66:67]
	v_pk_fma_f16 v101, v64, s36, v62 op_sel_hi:[1,0,1]
	s_add_u32 s66, s26, s64
	s_addc_u32 s67, s27, s65
	global_load_dwordx2 v[64:65], v121, s[66:67]
	v_pk_fma_f16 v102, v63, s36, v61 op_sel_hi:[1,0,1]
	s_add_u32 s66, s28, s64
	s_addc_u32 s67, s29, s65
	global_load_dwordx2 v[62:63], v121, s[66:67]
	s_add_u32 s66, s34, s64
	s_addc_u32 s67, s35, s65
	global_load_dwordx2 v[60:61], v121, s[66:67]
	v_pk_fma_f16 v97, v59, s36, v58 op_sel_hi:[1,0,1]
	s_add_u32 s66, s38, s64
	s_addc_u32 s67, s39, s65
	global_load_dwordx2 v[58:59], v121, s[66:67]
	v_pk_fma_f16 v98, v57, s36, v56 op_sel_hi:[1,0,1]
	s_add_u32 s66, s50, s64
	s_addc_u32 s67, s51, s65
	global_load_dwordx2 v[56:57], v121, s[66:67]
	v_pk_fma_f16 v99, v52, s36, v54 op_sel_hi:[1,0,1]
	s_add_u32 s66, s52, s64
	s_addc_u32 s67, s53, s65
	global_load_dwordx2 v[54:55], v121, s[66:67]
	s_add_u32 s66, s54, s64
	s_addc_u32 s67, s55, s65
	global_load_dwordx2 v[52:53], v121, s[66:67]
	s_nop 0
	s_nop 0
	s_nop 0
	s_nop 0
	s_nop 0
	s_nop 0
	s_nop 0
	s_cmpk_eq_i32 s58, 0x90
	s_cbranch_scc0 .LBB0_763
	v_lshlrev_b64 v[0:1], 2, v[2:3]
	v_lshl_add_u64 v[2:3], v[28:29], 0, v[0:1]
	v_mov_b32_e32 v104, v208
	v_mov_b32_e32 v105, v209
	v_mov_b32_e32 v106, v210
	v_mov_b32_e32 v107, v211
	v_mov_b32_e32 v108, v212
	v_mov_b32_e32 v109, v213
	v_mov_b32_e32 v110, v214
	v_mov_b32_e32 v111, v215
	v_mov_b32_e32 v86, v216
	v_mov_b32_e32 v87, v217
	v_mov_b32_e32 v88, v218
	v_mov_b32_e32 v89, v219
	v_mov_b32_e32 v112, v220
	v_mov_b32_e32 v113, v221
	v_mov_b32_e32 v114, v222
	v_mov_b32_e32 v115, v223
	v_lshl_add_u64 v[72:73], v[32:33], 0, v[0:1]
	v_cvt_f32_f16_sdwa v1, v103 dst_sel:DWORD dst_unused:UNUSED_PAD src0_sel:WORD_1
	v_cvt_f32_f16_e32 v0, v103
	v_cvt_f32_f16_sdwa v91, v102 dst_sel:DWORD dst_unused:UNUSED_PAD src0_sel:WORD_1
	v_cvt_f32_f16_e32 v90, v102
	v_cvt_f32_f16_sdwa v103, v101 dst_sel:DWORD dst_unused:UNUSED_PAD src0_sel:WORD_1
	v_cvt_f32_f16_e32 v102, v101
	v_cvt_f32_f16_sdwa v101, v100 dst_sel:DWORD dst_unused:UNUSED_PAD src0_sel:WORD_1
	v_cvt_f32_f16_e32 v100, v100
	s_mov_b32 s18, 0x800000
	v_readlane_b32 s12, v255, 5
	v_readlane_b32 s13, v255, 6
	v_pk_add_f32 v[86:87], v[86:87], v[102:103]
	v_pk_add_f32 v[84:85], v[112:113], v[0:1]
	v_mov_b32_e32 v102, v85
	v_mov_b32_e32 v103, v87
	v_pk_add_f32 v[90:91], v[114:115], v[90:91]
	v_pk_add_f32 v[88:89], v[88:89], v[100:101]
	v_mov_b32_e32 v100, v84
	v_mov_b32_e32 v101, v86
	v_pk_mul_f32 v[102:103], v[102:103], v[102:103]
	v_mov_b32_e32 v112, v91
	v_pk_fma_f32 v[100:101], v[100:101], v[100:101], v[102:103]
	v_mov_b32_e32 v102, v90
	v_mov_b32_e32 v103, v88
	v_pk_fma_f32 v[100:101], v[102:103], v[102:103], v[100:101]
	v_cvt_f32_f16_sdwa v103, v99 dst_sel:DWORD dst_unused:UNUSED_PAD src0_sel:WORD_1
	v_cvt_f32_f16_e32 v102, v99
	v_cvt_f32_f16_sdwa v99, v98 dst_sel:DWORD dst_unused:UNUSED_PAD src0_sel:WORD_1
	v_cvt_f32_f16_e32 v98, v98
	v_mov_b32_e32 v113, v89
	v_pk_add_f32 v[102:103], v[108:109], v[102:103]
	v_cvt_f32_f16_sdwa v109, v97 dst_sel:DWORD dst_unused:UNUSED_PAD src0_sel:WORD_1
	v_cvt_f32_f16_e32 v108, v97
	v_cvt_f32_f16_sdwa v97, v96 dst_sel:DWORD dst_unused:UNUSED_PAD src0_sel:WORD_1
	v_cvt_f32_f16_e32 v96, v96
	v_pk_add_f32 v[98:99], v[110:111], v[98:99]
	v_pk_add_f32 v[104:105], v[104:105], v[108:109]
	v_mov_b32_e32 v108, v103
	v_mov_b32_e32 v109, v105
	v_pk_add_f32 v[96:97], v[106:107], v[96:97]
	v_mov_b32_e32 v106, v102
	v_mov_b32_e32 v107, v104
	v_pk_mul_f32 v[108:109], v[108:109], v[108:109]
	v_pk_fma_f32 v[100:101], v[112:113], v[112:113], v[100:101]
	v_pk_fma_f32 v[106:107], v[106:107], v[106:107], v[108:109]
	v_mov_b32_e32 v108, v98
	v_mov_b32_e32 v109, v96
	v_mov_b32_e32 v110, v99
	v_mov_b32_e32 v111, v97
	v_pk_fma_f32 v[106:107], v[108:109], v[108:109], v[106:107]
	v_add_f32_e32 v95, v100, v101
	v_pk_fma_f32 v[106:107], v[110:111], v[110:111], v[106:107]
	v_lshl_add_u64 v[34:35], v[34:35], 0, s[12:13]
	v_add_f32_e32 v95, v95, v106
	v_add_f32_e32 v95, v95, v107
	v_mov_b32_e32 v100, v95
	s_nop 1
	v_permlane32_swap_b32 v100, v95
	s_waitcnt lgkmcnt(0)
	v_add_f32_e32 v95, v95, v100
	v_mov_b32_e32 v100, v95
	s_nop 1
	v_permlane16_swap_b32 v100, v95
	s_waitcnt lgkmcnt(0)
	v_add_f32_e32 v95, v95, v100
	s_nop 1
	v_mov_b32_dpp v100, v95 row_ror:8 row_mask:0xf bank_mask:0xf
	s_waitcnt lgkmcnt(0)
	v_add_f32_e32 v95, v95, v100
	s_nop 1
	v_mov_b32_dpp v100, v95 row_half_mirror row_mask:0xf bank_mask:0xf
	s_nop 1
	v_mov_b32_dpp v100, v100 quad_perm:[3,2,1,0] row_mask:0xf bank_mask:0xf
	s_waitcnt lgkmcnt(0)
	v_add_f32_e32 v95, v95, v100
	s_nop 1
	v_mov_b32_dpp v100, v95 quad_perm:[2,3,0,1] row_mask:0xf bank_mask:0xf
	s_waitcnt lgkmcnt(0)
	v_add_f32_e32 v95, v95, v100
	s_nop 1
	v_mov_b32_dpp v100, v95 quad_perm:[1,0,3,2] row_mask:0xf bank_mask:0xf
	s_waitcnt lgkmcnt(0)
	v_add_f32_e32 v95, v95, v100
	v_fmamk_f32 v95, v95, 0x3a800000, v191
	v_cmp_gt_f32_e32 vcc, s18, v95
	v_mul_f32_e32 v100, 0x4b800000, v95
	s_nop 0
	v_cndmask_b32_e32 v95, v95, v100, vcc
	v_rsq_f32_e32 v95, v95
	s_nop 0
	v_mul_f32_e32 v100, 0x45800000, v95
	v_cndmask_b32_e32 v100, v95, v100, vcc
	v_pk_mul_f32 v[84:85], v[84:85], v[100:101] op_sel_hi:[1,0]
	v_pk_mul_f32 v[0:1], v[124:125], v[84:85]
	v_pk_mul_f32 v[84:85], v[90:91], v[100:101] op_sel_hi:[1,0]
	s_nop 0
	v_pk_mul_f32 v[2:3], v[126:127], v[84:85]
	global_store_dwordx4 v[72:73], v[0:3], off
	s_nop 1
	v_pk_mul_f32 v[84:85], v[86:87], v[100:101] op_sel_hi:[1,0]
	v_pk_mul_f32 v[0:1], v[128:129], v[84:85]
	v_pk_mul_f32 v[84:85], v[88:89], v[100:101] op_sel_hi:[1,0]
	s_nop 0
	v_pk_mul_f32 v[2:3], v[130:131], v[84:85]
	global_store_dwordx4 v[72:73], v[0:3], off offset:16
	s_nop 1
	v_pk_mul_f32 v[84:85], v[102:103], v[100:101] op_sel_hi:[1,0]
	v_pk_mul_f32 v[0:1], v[84:85], v[132:133]
	v_pk_mul_f32 v[84:85], v[98:99], v[100:101] op_sel_hi:[1,0]
	s_nop 0
	v_pk_mul_f32 v[2:3], v[84:85], v[134:135]
	global_store_dwordx4 v[72:73], v[0:3], off offset:32
	s_nop 1
	v_pk_mul_f32 v[84:85], v[104:105], v[100:101] op_sel_hi:[1,0]
	v_pk_mul_f32 v[0:1], v[84:85], v[136:137]
	v_pk_mul_f32 v[84:85], v[96:97], v[100:101] op_sel_hi:[1,0]
	s_nop 0
	v_pk_mul_f32 v[2:3], v[84:85], v[138:139]
	global_store_dwordx4 v[72:73], v[0:3], off offset:48
	s_nop 1
	v_mov_b32_e32 v0, v94
	s_andn2_b64 exec, exec, s[10:11]
	s_cbranch_execnz .LBB0_762

.LBB0_770:
	s_cmpk_ge_i32 s56, 0x70
	s_cselect_b64 s[10:11], -1, 0
	ds_bpermute_b32 v6, v97, v96
	s_and_b64 vcc, s[10:11], s[48:49]
	v_cndmask_b32_e32 v94, v0, v98, vcc
	v_ashrrev_i32_e32 v95, 31, v94
	s_add_i32 s10, s56, 16
	s_and_b32 s10, s10, 0x70
	v_lshlrev_b64 v[94:95], 9, v[94:95]
	v_lshl_add_u64 v[94:95], s[94:95], 0, v[94:95]
	s_lshl_b32 s36, s10, 2
	s_waitcnt lgkmcnt(0)
	s_waitcnt vmcnt(32)
	v_mov_b32_e32 v96, v122
	v_ashrrev_i32_e32 v7, 31, v6
	v_lshl_add_u64 v[94:95], v[94:95], 0, s[36:37]
	v_lshl_add_u64 v[6:7], v[6:7], 3, s[88:89]
	v_lshl_add_u64 v[94:95], v[94:95], 0, v[144:145]
	global_load_dwordx2 v[6:7], v[6:7], off
	s_nop 0
	global_load_dword v8, v[4:5], off
	global_load_dword v122, v[94:95], off
	s_waitcnt vmcnt(19)
	v_dot8_i32_i4 v9, v20, v1, 0
	v_dot8_i32_i4 v94, v20, v10, 0
	v_dot8_i32_i4 v9, v21, v11, v9
	v_dot8_i32_i4 v94, v21, v12, v94
	v_dot8_i32_i4 v20, v22, v1, 0
	v_dot8_i32_i4 v21, v22, v10, 0
	v_dot8_i32_i4 v20, v23, v11, v20
	v_dot8_i32_i4 v21, v23, v12, v21
	v_lshl_add_u32 v9, v9, 4, v94
	s_add_i32 s56, s56, 16
	s_nop 0
	v_lshl_add_u32 v94, v20, 4, v21
	s_waitcnt vmcnt(19)
	v_dot8_i32_i4 v20, v24, v1, 0
	v_dot8_i32_i4 v21, v24, v10, 0
	v_dot8_i32_i4 v20, v25, v11, v20
	v_dot8_i32_i4 v21, v25, v12, v21
	v_lshl_add_u64 v[4:5], v[4:5], 0, 64
	s_nop 1
	v_lshl_add_u32 v95, v20, 4, v21
	v_dot8_i32_i4 v20, v26, v1, 0
	v_dot8_i32_i4 v21, v26, v10, 0
	v_dot8_i32_i4 v20, v27, v11, v20
	v_dot8_i32_i4 v21, v27, v12, v21
	v_readlane_b32 s10, v96, 0
	s_ashr_i32 s11, s10, 31
	v_readlane_b32 s12, v96, 1
	v_lshl_add_u32 v106, v20, 4, v21
	v_dot8_i32_i4 v20, v28, v1, 0
	v_dot8_i32_i4 v21, v28, v10, 0
	v_dot8_i32_i4 v20, v29, v11, v20
	v_dot8_i32_i4 v21, v29, v12, v21
	s_lshl_b64 s[10:11], s[10:11], 9
	s_ashr_i32 s13, s12, 31
	v_readlane_b32 s14, v96, 2
	v_lshl_add_u32 v107, v20, 4, v21
	v_dot8_i32_i4 v20, v30, v1, 0
	v_dot8_i32_i4 v21, v30, v10, 0
	v_dot8_i32_i4 v20, v31, v11, v20
	v_dot8_i32_i4 v21, v31, v12, v21
	s_lshl_b64 s[12:13], s[12:13], 9
	s_ashr_i32 s15, s14, 31
	v_readlane_b32 s16, v96, 3
	v_lshl_add_u32 v108, v20, 4, v21
	v_dot8_i32_i4 v20, v32, v1, 0
	v_dot8_i32_i4 v21, v32, v10, 0
	v_dot8_i32_i4 v20, v33, v11, v20
	v_dot8_i32_i4 v21, v33, v12, v21
	s_lshl_b64 s[14:15], s[14:15], 9
	s_ashr_i32 s17, s16, 31
	s_nop 0
	v_lshl_add_u32 v109, v20, 4, v21
	v_dot8_i32_i4 v20, v34, v1, 0
	v_dot8_i32_i4 v21, v34, v10, 0
	v_dot8_i32_i4 v20, v35, v11, v20
	v_dot8_i32_i4 v21, v35, v12, v21
	v_readlane_b32 s18, v96, 4
	s_add_u32 s66, s12, s62
	s_addc_u32 s67, s13, s63
	global_load_dwordx2 v[22:23], v121, s[66:67]
	v_lshl_add_u32 v110, v20, 4, v21
	v_dot8_i32_i4 v20, v36, v1, 0
	v_dot8_i32_i4 v21, v36, v10, 0
	v_dot8_i32_i4 v20, v37, v11, v20
	v_dot8_i32_i4 v21, v37, v12, v21
	s_lshl_b64 s[16:17], s[16:17], 9
	s_ashr_i32 s19, s18, 31
	v_readlane_b32 s20, v96, 5
	v_lshl_add_u32 v111, v20, 4, v21
	v_dot8_i32_i4 v20, v38, v1, 0
	v_dot8_i32_i4 v21, v38, v10, 0
	v_dot8_i32_i4 v20, v39, v11, v20
	v_dot8_i32_i4 v21, v39, v12, v21
	s_setprio 2
	v_permlane32_swap_b32 v9, v111
	s_nop 1
	v_lshl_add_u32 v112, v20, 4, v21
	v_dot8_i32_i4 v20, v40, v1, 0
	v_dot8_i32_i4 v21, v40, v10, 0
	v_dot8_i32_i4 v20, v41, v11, v20
	v_dot8_i32_i4 v21, v41, v12, v21
	s_waitcnt lgkmcnt(0)
	v_add_u32_e32 v9, v9, v111
	v_permlane32_swap_b32 v94, v112
	v_lshl_add_u32 v113, v20, 4, v21
	v_dot8_i32_i4 v20, v60, v1, 0
	v_dot8_i32_i4 v21, v60, v10, 0
	v_dot8_i32_i4 v20, v61, v11, v20
	v_dot8_i32_i4 v21, v61, v12, v21
	s_waitcnt lgkmcnt(0)
	v_add_u32_e32 v94, v94, v112
	v_permlane32_swap_b32 v95, v113
	v_lshl_add_u32 v114, v20, 4, v21
	v_dot8_i32_i4 v20, v58, v1, 0
	v_dot8_i32_i4 v21, v58, v10, 0
	v_dot8_i32_i4 v20, v59, v11, v20
	v_dot8_i32_i4 v21, v59, v12, v21
	s_waitcnt lgkmcnt(0)
	v_add_u32_e32 v95, v95, v113
	v_permlane32_swap_b32 v106, v114
	v_lshl_add_u32 v115, v20, 4, v21
	v_dot8_i32_i4 v20, v56, v1, 0
	v_dot8_i32_i4 v21, v56, v10, 0
	v_dot8_i32_i4 v20, v57, v11, v20
	v_dot8_i32_i4 v21, v57, v12, v21
	s_waitcnt lgkmcnt(0)
	v_add_u32_e32 v106, v106, v114
	v_permlane32_swap_b32 v107, v115
	v_lshl_add_u32 v116, v20, 4, v21
	v_dot8_i32_i4 v20, v54, v1, 0
	v_dot8_i32_i4 v21, v54, v10, 0
	v_dot8_i32_i4 v20, v55, v11, v20
	v_dot8_i32_i4 v21, v55, v12, v21
	s_waitcnt lgkmcnt(0)
	v_add_u32_e32 v107, v107, v115
	v_permlane32_swap_b32 v108, v116
	v_lshl_add_u32 v117, v20, 4, v21
	v_dot8_i32_i4 v20, v52, v1, 0
	v_dot8_i32_i4 v21, v52, v10, 0
	v_dot8_i32_i4 v20, v53, v11, v20
	v_dot8_i32_i4 v21, v53, v12, v21
	s_waitcnt lgkmcnt(0)
	v_add_u32_e32 v108, v108, v116
	v_permlane32_swap_b32 v109, v117
	v_lshl_add_u32 v118, v20, 4, v21
	s_waitcnt lgkmcnt(0)
	v_add_u32_e32 v109, v109, v117
	v_permlane32_swap_b32 v110, v118
	s_add_u32 s66, s10, s62
	s_addc_u32 s67, s11, s63
	global_load_dwordx2 v[20:21], v121, s[66:67]
	s_add_u32 s66, s14, s62
	s_addc_u32 s67, s15, s63
	global_load_dwordx2 v[24:25], v121, s[66:67]
	s_waitcnt lgkmcnt(0)
	v_add_u32_e32 v110, v110, v118
	v_permlane16_swap_b32 v9, v107
	s_lshl_b64 s[18:19], s[18:19], 9
	s_ashr_i32 s21, s20, 31
	v_readlane_b32 s22, v96, 6
	s_add_u32 s66, s16, s62
	s_addc_u32 s67, s17, s63
	global_load_dwordx2 v[26:27], v121, s[66:67]
	s_waitcnt lgkmcnt(0)
	v_add_u32_e32 v9, v9, v107
	v_permlane16_swap_b32 v94, v108
	s_lshl_b64 s[20:21], s[20:21], 9
	s_ashr_i32 s23, s22, 31
	s_waitcnt lgkmcnt(0)
	v_add_u32_e32 v94, v94, v108
	v_permlane16_swap_b32 v95, v109
	v_readlane_b32 s24, v96, 7
	s_add_u32 s66, s18, s62
	s_addc_u32 s67, s19, s63
	global_load_dwordx2 v[28:29], v121, s[66:67]
	s_waitcnt lgkmcnt(0)
	v_add_u32_e32 v95, v95, v109
	v_permlane16_swap_b32 v106, v110
	s_lshl_b64 s[22:23], s[22:23], 9
	s_ashr_i32 s25, s24, 31
	v_readlane_b32 s26, v96, 8
	s_waitcnt lgkmcnt(0)
	v_add_u32_e32 v106, v106, v110
	v_cndmask_b32_e64 v107, v9, v95, s[44:45]
	v_cndmask_b32_e64 v9, v95, v9, s[44:45]
	s_nop 0
	s_add_u32 s66, s20, s62
	s_addc_u32 s67, s21, s63
	global_load_dwordx2 v[30:31], v121, s[66:67]
	s_lshl_b64 s[24:25], s[24:25], 9
	s_ashr_i32 s27, s26, 31
	s_waitcnt lgkmcnt(0)
	v_add_u32_dpp v9, v107, v9 row_ror:8 row_mask:0xf bank_mask:0xf
	v_cndmask_b32_e64 v95, v94, v106, s[44:45]
	s_nop 1
	v_cndmask_b32_e64 v94, v106, v94, s[44:45]
	v_readlane_b32 s28, v96, 9
	s_add_u32 s66, s22, s62
	s_addc_u32 s67, s23, s63
	global_load_dwordx2 v[32:33], v121, s[66:67]
	s_waitcnt lgkmcnt(0)
	v_add_u32_dpp v94, v95, v94 row_ror:8 row_mask:0xf bank_mask:0xf
	v_cndmask_b32_e64 v95, v9, v94, s[46:47]
	v_cndmask_b32_e64 v9, v94, v9, s[46:47]
	s_nop 0
	v_mov_b32_dpp v94, v95 row_half_mirror row_mask:0xf bank_mask:0xf
	s_nop 1
	s_lshl_b64 s[26:27], s[26:27], 9
	s_ashr_i32 s29, s28, 31
	v_readlane_b32 s30, v96, 10
	s_add_u32 s66, s24, s62
	s_addc_u32 s67, s25, s63
	global_load_dwordx2 v[34:35], v121, s[66:67]
	s_waitcnt lgkmcnt(0)
	v_add_u32_dpp v9, v94, v9 quad_perm:[3,2,1,0] row_mask:0xf bank_mask:0xf
	s_nop 1
	s_lshl_b64 s[28:29], s[28:29], 9
	s_ashr_i32 s31, s30, 31
	v_readlane_b32 s34, v96, 11
	s_waitcnt lgkmcnt(0)
	v_add_u32_dpp v9, v9, v9 quad_perm:[2,3,0,1] row_mask:0xf bank_mask:0xf
	s_nop 1
	s_add_u32 s66, s26, s62
	s_addc_u32 s67, s27, s63
	global_load_dwordx2 v[36:37], v121, s[66:67]
	s_lshl_b64 s[30:31], s[30:31], 9
	s_ashr_i32 s35, s34, 31
	s_waitcnt lgkmcnt(0)
	v_add_u32_dpp v9, v9, v9 quad_perm:[1,0,3,2] row_mask:0xf bank_mask:0xf
	s_waitcnt vmcnt(10)
	v_mul_f32_e32 v7, v13, v7
	v_cvt_f32_i32_e32 v9, v9
	v_add_f32_e32 v9, v14, v9
	v_mul_f32_e32 v7, v7, v9
	v_mul_f32_e32 v9, 0x3d372713, v7
	v_mul_f32_e32 v9, v7, v9
	v_fma_f32 v9, v7, v9, v7
	v_mul_f32_e32 v9, 0x3fcc422a, v9
	v_mul_f32_e32 v9, 0xbfb8aa3b, v9
	v_exp_f32_e32 v9, v9
	v_readlane_b32 s38, v96, 12
	s_add_u32 s66, s28, s62
	s_addc_u32 s67, s29, s63
	global_load_dwordx2 v[38:39], v121, s[66:67]
	v_add_f32_e32 v9, 1.0, v9
	v_rcp_f32_e32 v9, v9
	s_lshl_b64 s[34:35], s[34:35], 9
	s_ashr_i32 s39, s38, 31
	s_lshl_b64 s[38:39], s[38:39], 9
	v_readlane_b32 s50, v96, 13
	v_readlane_b32 s52, v96, 14
	v_readlane_b32 s54, v96, 15
	s_ashr_i32 s51, s50, 31
	s_ashr_i32 s53, s52, 31
	s_ashr_i32 s55, s54, 31
	s_lshl_b64 s[50:51], s[50:51], 9
	s_lshl_b64 s[52:53], s[52:53], 9
	s_lshl_b64 s[54:55], s[54:55], 9
	s_add_u32 s66, s30, s62
	s_addc_u32 s67, s31, s63
	global_load_dwordx2 v[40:41], v121, s[66:67]
	s_add_u32 s66, s34, s62
	s_addc_u32 s67, s35, s63
	global_load_dwordx2 v[60:61], v121, s[66:67]
	s_add_u32 s66, s38, s62
	s_addc_u32 s67, s39, s63
	global_load_dwordx2 v[58:59], v121, s[66:67]
	s_add_u32 s66, s50, s62
	s_addc_u32 s67, s51, s63
	global_load_dwordx2 v[56:57], v121, s[66:67]
	s_add_u32 s66, s52, s62
	s_addc_u32 s67, s53, s63
	global_load_dwordx2 v[54:55], v121, s[66:67]
	s_add_u32 s66, s54, s62
	s_addc_u32 s67, s55, s63
	global_load_dwordx2 v[52:53], v121, s[66:67]
	v_pk_mul_f32 v[6:7], v[6:7], v[8:9]
	s_waitcnt vmcnt(34)
	v_alignbit_b32 v224, v92, v92, 4
	v_pk_mul_f32 v[6:7], v[6:7], v[6:7] op_sel:[0,1] op_sel_hi:[1,0]
	v_cvt_f16_f32_e32 v120, v6
	s_setprio 0
	v_and_b32_e32 v8, 0x7070707, v92
	v_readlane_b32 s36, v120, 0
	v_and_b32_e32 v9, 0x7070707, v224
	v_perm_b32 v8, s2, v205, v8
	v_perm_b32 v9, s2, v205, v9
	v_and_or_b32 v8, v92, s4, v8
	v_and_or_b32 v9, v224, s4, v9
	v_perm_b32 v92, v9, v8, s5
	v_perm_b32 v94, v9, v8, s33
	v_perm_b32 v95, v9, v8, s0
	v_perm_b32 v8, v9, v8, s1
	v_pk_fma_f16 v8, v8, s36, v102 op_sel_hi:[1,0,1]
	v_alignbit_b32 v225, v93, v93, 4
	v_pk_fma_f16 v9, v92, s36, v105 op_sel_hi:[1,0,1]
	v_pk_fma_f16 v92, v94, s36, v104 op_sel_hi:[1,0,1]
	v_pk_fma_f16 v94, v95, s36, v103 op_sel_hi:[1,0,1]
	v_and_b32_e32 v95, 0x7070707, v93
	v_and_b32_e32 v102, 0x7070707, v225
	v_perm_b32 v95, s2, v205, v95
	v_perm_b32 v102, s2, v205, v102
	v_and_or_b32 v95, v93, s4, v95
	v_and_or_b32 v93, v225, s4, v102
	v_perm_b32 v102, v93, v95, s5
	v_perm_b32 v103, v93, v95, s33
	v_perm_b32 v104, v93, v95, s0
	v_perm_b32 v93, v93, v95, s1
	v_pk_fma_f16 v95, v102, s36, v101 op_sel_hi:[1,0,1]
	v_readlane_b32 s59, v120, 4
	s_waitcnt vmcnt(33)
	v_alignbit_b32 v224, v90, v90, 4
	v_pk_fma_f16 v100, v103, s36, v100 op_sel_hi:[1,0,1]
	v_pk_fma_f16 v99, v104, s36, v99 op_sel_hi:[1,0,1]
	v_pk_fma_f16 v7, v93, s36, v15 op_sel_hi:[1,0,1]
	v_and_b32_e32 v93, 0x7070707, v90
	v_and_b32_e32 v101, 0x7070707, v224
	v_perm_b32 v93, s2, v205, v93
	v_perm_b32 v101, s2, v205, v101
	v_and_or_b32 v93, v90, s4, v93
	v_and_or_b32 v90, v224, s4, v101
	v_perm_b32 v103, v90, v93, s0
	v_perm_b32 v101, v90, v93, s5
	v_perm_b32 v102, v90, v93, s33
	v_perm_b32 v90, v90, v93, s1
	v_pk_fma_f16 v93, v103, s59, v94 op_sel_hi:[1,0,1]
	v_alignbit_b32 v225, v91, v91, 4
	v_pk_fma_f16 v8, v90, s59, v8 op_sel_hi:[1,0,1]
	v_and_b32_e32 v90, 0x7070707, v91
	v_and_b32_e32 v94, 0x7070707, v225
	v_pk_fma_f16 v9, v101, s59, v9 op_sel_hi:[1,0,1]
	v_perm_b32 v90, s2, v205, v90
	v_perm_b32 v94, s2, v205, v94
	v_and_or_b32 v90, v91, s4, v90
	v_and_or_b32 v91, v225, s4, v94
	v_pk_fma_f16 v92, v102, s59, v92 op_sel_hi:[1,0,1]
	v_perm_b32 v94, v91, v90, s5
	v_perm_b32 v102, v91, v90, s0
	v_perm_b32 v101, v91, v90, s33
	v_perm_b32 v90, v91, v90, s1
	v_pk_fma_f16 v91, v94, s59, v95 op_sel_hi:[1,0,1]
	v_pk_fma_f16 v95, v102, s59, v99 op_sel_hi:[1,0,1]
	v_readlane_b32 s60, v120, 8
	s_waitcnt vmcnt(32)
	v_alignbit_b32 v224, v88, v88, 4
	v_pk_fma_f16 v94, v101, s59, v100 op_sel_hi:[1,0,1]
	v_pk_fma_f16 v7, v90, s59, v7 op_sel_hi:[1,0,1]
	v_and_b32_e32 v90, 0x7070707, v88
	v_and_b32_e32 v99, 0x7070707, v224
	v_perm_b32 v90, s2, v205, v90
	v_perm_b32 v99, s2, v205, v99
	v_and_or_b32 v90, v88, s4, v90
	v_and_or_b32 v88, v224, s4, v99
	v_perm_b32 v100, v88, v90, s33
	v_perm_b32 v101, v88, v90, s0
	v_perm_b32 v99, v88, v90, s5
	v_perm_b32 v88, v88, v90, s1
	v_pk_fma_f16 v90, v100, s60, v92 op_sel_hi:[1,0,1]
	v_pk_fma_f16 v92, v101, s60, v93 op_sel_hi:[1,0,1]
	v_alignbit_b32 v225, v89, v89, 4
	v_pk_fma_f16 v8, v88, s60, v8 op_sel_hi:[1,0,1]
	v_and_b32_e32 v88, 0x7070707, v89
	v_and_b32_e32 v93, 0x7070707, v225
	v_pk_fma_f16 v9, v99, s60, v9 op_sel_hi:[1,0,1]
	v_perm_b32 v88, s2, v205, v88
	v_perm_b32 v93, s2, v205, v93
	v_and_or_b32 v88, v89, s4, v88
	v_and_or_b32 v89, v225, s4, v93
	v_perm_b32 v93, v89, v88, s5
	v_perm_b32 v99, v89, v88, s33
	v_perm_b32 v100, v89, v88, s0
	v_perm_b32 v88, v89, v88, s1
	v_pk_fma_f16 v89, v93, s60, v91 op_sel_hi:[1,0,1]
	v_pk_fma_f16 v91, v99, s60, v94 op_sel_hi:[1,0,1]
	v_readlane_b32 s36, v120, 12
	s_waitcnt vmcnt(31)
	v_alignbit_b32 v224, v86, v86, 4
	v_pk_fma_f16 v93, v100, s60, v95 op_sel_hi:[1,0,1]
	v_pk_fma_f16 v7, v88, s60, v7 op_sel_hi:[1,0,1]
	v_and_b32_e32 v88, 0x7070707, v86
	v_and_b32_e32 v94, 0x7070707, v224
	v_perm_b32 v88, s2, v205, v88
	v_perm_b32 v94, s2, v205, v94
	v_and_or_b32 v88, v86, s4, v88
	v_and_or_b32 v86, v224, s4, v94
	v_perm_b32 v95, v86, v88, s33
	v_perm_b32 v99, v86, v88, s0
	v_perm_b32 v94, v86, v88, s5
	v_perm_b32 v86, v86, v88, s1
	v_pk_fma_f16 v88, v95, s36, v90 op_sel_hi:[1,0,1]
	v_pk_fma_f16 v90, v99, s36, v92 op_sel_hi:[1,0,1]
	v_alignbit_b32 v225, v87, v87, 4
	v_pk_fma_f16 v8, v86, s36, v8 op_sel_hi:[1,0,1]
	v_and_b32_e32 v86, 0x7070707, v87
	v_and_b32_e32 v92, 0x7070707, v225
	v_pk_fma_f16 v9, v94, s36, v9 op_sel_hi:[1,0,1]
	v_perm_b32 v86, s2, v205, v86
	v_perm_b32 v92, s2, v205, v92
	v_and_or_b32 v86, v87, s4, v86
	v_and_or_b32 v87, v225, s4, v92
	v_perm_b32 v92, v87, v86, s5
	v_perm_b32 v94, v87, v86, s33
	v_perm_b32 v95, v87, v86, s0
	v_perm_b32 v86, v87, v86, s1
	v_pk_fma_f16 v87, v92, s36, v89 op_sel_hi:[1,0,1]
	v_readlane_b32 s59, v120, 16
	s_waitcnt vmcnt(30)
	v_alignbit_b32 v224, v84, v84, 4
	v_pk_fma_f16 v89, v94, s36, v91 op_sel_hi:[1,0,1]
	v_pk_fma_f16 v91, v95, s36, v93 op_sel_hi:[1,0,1]
	v_pk_fma_f16 v7, v86, s36, v7 op_sel_hi:[1,0,1]
	v_and_b32_e32 v86, 0x7070707, v84
	v_and_b32_e32 v92, 0x7070707, v224
	v_perm_b32 v86, s2, v205, v86
	v_perm_b32 v92, s2, v205, v92
	v_and_or_b32 v86, v84, s4, v86
	v_and_or_b32 v84, v224, s4, v92
	v_perm_b32 v93, v84, v86, s33
	v_perm_b32 v94, v84, v86, s0
	v_perm_b32 v92, v84, v86, s5
	v_perm_b32 v84, v84, v86, s1
	v_pk_fma_f16 v86, v93, s59, v88 op_sel_hi:[1,0,1]
	v_pk_fma_f16 v88, v94, s59, v90 op_sel_hi:[1,0,1]
	v_alignbit_b32 v225, v85, v85, 4
	v_pk_fma_f16 v8, v84, s59, v8 op_sel_hi:[1,0,1]
	v_and_b32_e32 v84, 0x7070707, v85
	v_and_b32_e32 v90, 0x7070707, v225
	v_pk_fma_f16 v9, v92, s59, v9 op_sel_hi:[1,0,1]
	v_perm_b32 v84, s2, v205, v84
	v_perm_b32 v90, s2, v205, v90
	v_and_or_b32 v84, v85, s4, v84
	v_and_or_b32 v85, v225, s4, v90
	v_perm_b32 v90, v85, v84, s5
	v_perm_b32 v92, v85, v84, s33
	v_perm_b32 v93, v85, v84, s0
	v_perm_b32 v84, v85, v84, s1
	v_pk_fma_f16 v85, v90, s59, v87 op_sel_hi:[1,0,1]
	v_readlane_b32 s60, v120, 20
	s_waitcnt vmcnt(29)
	v_alignbit_b32 v224, v82, v82, 4
	v_pk_fma_f16 v87, v92, s59, v89 op_sel_hi:[1,0,1]
	v_pk_fma_f16 v89, v93, s59, v91 op_sel_hi:[1,0,1]
	v_pk_fma_f16 v7, v84, s59, v7 op_sel_hi:[1,0,1]
	v_and_b32_e32 v84, 0x7070707, v82
	v_and_b32_e32 v90, 0x7070707, v224
	v_perm_b32 v84, s2, v205, v84
	v_perm_b32 v90, s2, v205, v90
	v_and_or_b32 v84, v82, s4, v84
	v_and_or_b32 v82, v224, s4, v90
	v_perm_b32 v91, v82, v84, s33
	v_perm_b32 v92, v82, v84, s0
	v_perm_b32 v90, v82, v84, s5
	v_perm_b32 v82, v82, v84, s1
	v_pk_fma_f16 v84, v91, s60, v86 op_sel_hi:[1,0,1]
	v_pk_fma_f16 v86, v92, s60, v88 op_sel_hi:[1,0,1]
	s_add_u32 s66, s10, s64
	s_addc_u32 s67, s11, s65
	global_load_dwordx2 v[92:93], v121, s[66:67]
	v_alignbit_b32 v225, v83, v83, 4
	v_pk_fma_f16 v8, v82, s60, v8 op_sel_hi:[1,0,1]
	v_and_b32_e32 v82, 0x7070707, v83
	v_and_b32_e32 v88, 0x7070707, v225
	v_pk_fma_f16 v9, v90, s60, v9 op_sel_hi:[1,0,1]
	v_perm_b32 v82, s2, v205, v82
	v_perm_b32 v88, s2, v205, v88
	v_and_or_b32 v82, v83, s4, v82
	v_and_or_b32 v83, v225, s4, v88
	v_perm_b32 v88, v83, v82, s5
	v_perm_b32 v90, v83, v82, s33
	v_perm_b32 v91, v83, v82, s0
	v_perm_b32 v82, v83, v82, s1
	v_pk_fma_f16 v83, v88, s60, v85 op_sel_hi:[1,0,1]
	v_readlane_b32 s36, v120, 24
	s_waitcnt vmcnt(29)
	v_alignbit_b32 v224, v80, v80, 4
	v_pk_fma_f16 v85, v90, s60, v87 op_sel_hi:[1,0,1]
	v_pk_fma_f16 v87, v91, s60, v89 op_sel_hi:[1,0,1]
	v_pk_fma_f16 v7, v82, s60, v7 op_sel_hi:[1,0,1]
	v_and_b32_e32 v82, 0x7070707, v80
	v_and_b32_e32 v88, 0x7070707, v224
	v_perm_b32 v82, s2, v205, v82
	v_perm_b32 v88, s2, v205, v88
	v_and_or_b32 v82, v80, s4, v82
	v_and_or_b32 v80, v224, s4, v88
	v_perm_b32 v89, v80, v82, s33
	v_perm_b32 v90, v80, v82, s0
	v_perm_b32 v88, v80, v82, s5
	v_perm_b32 v80, v80, v82, s1
	v_pk_fma_f16 v82, v89, s36, v84 op_sel_hi:[1,0,1]
	v_pk_fma_f16 v84, v90, s36, v86 op_sel_hi:[1,0,1]
	s_add_u32 s66, s12, s64
	s_addc_u32 s67, s13, s65
	global_load_dwordx2 v[90:91], v121, s[66:67]
	v_alignbit_b32 v225, v81, v81, 4
	v_pk_fma_f16 v8, v80, s36, v8 op_sel_hi:[1,0,1]
	v_and_b32_e32 v80, 0x7070707, v81
	v_and_b32_e32 v86, 0x7070707, v225
	v_pk_fma_f16 v9, v88, s36, v9 op_sel_hi:[1,0,1]
	v_perm_b32 v80, s2, v205, v80
	v_perm_b32 v86, s2, v205, v86
	v_and_or_b32 v80, v81, s4, v80
	v_and_or_b32 v81, v225, s4, v86
	v_perm_b32 v86, v81, v80, s5
	v_perm_b32 v88, v81, v80, s33
	v_perm_b32 v89, v81, v80, s0
	v_perm_b32 v80, v81, v80, s1
	v_pk_fma_f16 v81, v86, s36, v83 op_sel_hi:[1,0,1]
	v_readlane_b32 s59, v120, 28
	s_waitcnt vmcnt(29)
	v_alignbit_b32 v224, v78, v78, 4
	v_pk_fma_f16 v83, v88, s36, v85 op_sel_hi:[1,0,1]
	v_pk_fma_f16 v85, v89, s36, v87 op_sel_hi:[1,0,1]
	v_pk_fma_f16 v7, v80, s36, v7 op_sel_hi:[1,0,1]
	v_and_b32_e32 v80, 0x7070707, v78
	v_and_b32_e32 v86, 0x7070707, v224
	v_perm_b32 v80, s2, v205, v80
	v_perm_b32 v86, s2, v205, v86
	v_and_or_b32 v80, v78, s4, v80
	v_and_or_b32 v78, v224, s4, v86
	v_perm_b32 v87, v78, v80, s33
	v_perm_b32 v88, v78, v80, s0
	v_perm_b32 v86, v78, v80, s5
	v_perm_b32 v78, v78, v80, s1
	v_pk_fma_f16 v80, v87, s59, v82 op_sel_hi:[1,0,1]
	v_pk_fma_f16 v82, v88, s59, v84 op_sel_hi:[1,0,1]
	s_add_u32 s66, s14, s64
	s_addc_u32 s67, s15, s65
	global_load_dwordx2 v[88:89], v121, s[66:67]
	v_alignbit_b32 v225, v79, v79, 4
	v_pk_fma_f16 v8, v78, s59, v8 op_sel_hi:[1,0,1]
	v_and_b32_e32 v78, 0x7070707, v79
	v_and_b32_e32 v84, 0x7070707, v225
	v_pk_fma_f16 v9, v86, s59, v9 op_sel_hi:[1,0,1]
	v_perm_b32 v78, s2, v205, v78
	v_perm_b32 v84, s2, v205, v84
	v_and_or_b32 v78, v79, s4, v78
	v_and_or_b32 v79, v225, s4, v84
	v_perm_b32 v84, v79, v78, s5
	v_perm_b32 v86, v79, v78, s33
	v_perm_b32 v87, v79, v78, s0
	v_perm_b32 v78, v79, v78, s1
	v_pk_fma_f16 v79, v84, s59, v81 op_sel_hi:[1,0,1]
	v_readlane_b32 s60, v120, 32
	s_waitcnt vmcnt(29)
	v_alignbit_b32 v224, v76, v76, 4
	v_pk_fma_f16 v81, v86, s59, v83 op_sel_hi:[1,0,1]
	v_pk_fma_f16 v83, v87, s59, v85 op_sel_hi:[1,0,1]
	v_pk_fma_f16 v7, v78, s59, v7 op_sel_hi:[1,0,1]
	v_and_b32_e32 v78, 0x7070707, v76
	v_and_b32_e32 v84, 0x7070707, v224
	v_perm_b32 v78, s2, v205, v78
	v_perm_b32 v84, s2, v205, v84
	v_and_or_b32 v78, v76, s4, v78
	v_and_or_b32 v76, v224, s4, v84
	v_perm_b32 v85, v76, v78, s33
	v_perm_b32 v86, v76, v78, s0
	v_perm_b32 v84, v76, v78, s5
	v_perm_b32 v76, v76, v78, s1
	v_pk_fma_f16 v78, v85, s60, v80 op_sel_hi:[1,0,1]
	v_pk_fma_f16 v80, v86, s60, v82 op_sel_hi:[1,0,1]
	s_add_u32 s66, s16, s64
	s_addc_u32 s67, s17, s65
	global_load_dwordx2 v[86:87], v121, s[66:67]
	v_alignbit_b32 v225, v77, v77, 4
	v_pk_fma_f16 v8, v76, s60, v8 op_sel_hi:[1,0,1]
	v_and_b32_e32 v76, 0x7070707, v77
	v_and_b32_e32 v82, 0x7070707, v225
	v_pk_fma_f16 v9, v84, s60, v9 op_sel_hi:[1,0,1]
	v_perm_b32 v76, s2, v205, v76
	v_perm_b32 v82, s2, v205, v82
	v_and_or_b32 v76, v77, s4, v76
	v_and_or_b32 v77, v225, s4, v82
	v_perm_b32 v82, v77, v76, s5
	v_perm_b32 v84, v77, v76, s33
	v_perm_b32 v85, v77, v76, s0
	v_perm_b32 v76, v77, v76, s1
	v_pk_fma_f16 v77, v82, s60, v79 op_sel_hi:[1,0,1]
	v_readlane_b32 s36, v120, 36
	s_waitcnt vmcnt(28)
	v_alignbit_b32 v224, v70, v70, 4
	v_pk_fma_f16 v79, v84, s60, v81 op_sel_hi:[1,0,1]
	v_pk_fma_f16 v81, v85, s60, v83 op_sel_hi:[1,0,1]
	v_pk_fma_f16 v7, v76, s60, v7 op_sel_hi:[1,0,1]
	v_and_b32_e32 v76, 0x7070707, v70
	v_and_b32_e32 v82, 0x7070707, v224
	v_perm_b32 v76, s2, v205, v76
	v_perm_b32 v82, s2, v205, v82
	v_and_or_b32 v76, v70, s4, v76
	v_and_or_b32 v70, v224, s4, v82
	v_perm_b32 v83, v70, v76, s33
	v_perm_b32 v84, v70, v76, s0
	v_perm_b32 v82, v70, v76, s5
	v_perm_b32 v70, v70, v76, s1
	v_pk_fma_f16 v76, v83, s36, v78 op_sel_hi:[1,0,1]
	v_pk_fma_f16 v78, v84, s36, v80 op_sel_hi:[1,0,1]
	s_add_u32 s66, s18, s64
	s_addc_u32 s67, s19, s65
	global_load_dwordx2 v[84:85], v121, s[66:67]
	v_alignbit_b32 v225, v71, v71, 4
	v_pk_fma_f16 v8, v70, s36, v8 op_sel_hi:[1,0,1]
	v_and_b32_e32 v70, 0x7070707, v71
	v_and_b32_e32 v80, 0x7070707, v225
	v_pk_fma_f16 v9, v82, s36, v9 op_sel_hi:[1,0,1]
	v_perm_b32 v70, s2, v205, v70
	v_perm_b32 v80, s2, v205, v80
	v_and_or_b32 v70, v71, s4, v70
	v_and_or_b32 v71, v225, s4, v80
	v_perm_b32 v80, v71, v70, s5
	v_perm_b32 v82, v71, v70, s33
	v_perm_b32 v83, v71, v70, s0
	v_perm_b32 v70, v71, v70, s1
	v_pk_fma_f16 v71, v80, s36, v77 op_sel_hi:[1,0,1]
	v_readlane_b32 s59, v120, 40
	s_waitcnt vmcnt(25)
	v_alignbit_b32 v224, v66, v66, 4
	v_pk_fma_f16 v77, v82, s36, v79 op_sel_hi:[1,0,1]
	v_pk_fma_f16 v79, v83, s36, v81 op_sel_hi:[1,0,1]
	v_pk_fma_f16 v7, v70, s36, v7 op_sel_hi:[1,0,1]
	v_and_b32_e32 v70, 0x7070707, v66
	v_and_b32_e32 v80, 0x7070707, v224
	v_perm_b32 v70, s2, v205, v70
	v_perm_b32 v80, s2, v205, v80
	v_and_or_b32 v70, v66, s4, v70
	v_and_or_b32 v66, v224, s4, v80
	v_perm_b32 v81, v66, v70, s33
	v_perm_b32 v82, v66, v70, s0
	v_perm_b32 v80, v66, v70, s5
	v_perm_b32 v66, v66, v70, s1
	v_pk_fma_f16 v70, v81, s59, v76 op_sel_hi:[1,0,1]
	v_pk_fma_f16 v76, v82, s59, v78 op_sel_hi:[1,0,1]
	s_add_u32 s66, s20, s64
	s_addc_u32 s67, s21, s65
	global_load_dwordx2 v[82:83], v121, s[66:67]
	v_alignbit_b32 v225, v67, v67, 4
	v_pk_fma_f16 v8, v66, s59, v8 op_sel_hi:[1,0,1]
	v_and_b32_e32 v66, 0x7070707, v67
	v_and_b32_e32 v78, 0x7070707, v225
	v_pk_fma_f16 v9, v80, s59, v9 op_sel_hi:[1,0,1]
	v_perm_b32 v66, s2, v205, v66
	v_perm_b32 v78, s2, v205, v78
	v_and_or_b32 v66, v67, s4, v66
	v_and_or_b32 v67, v225, s4, v78
	v_perm_b32 v78, v67, v66, s5
	v_perm_b32 v80, v67, v66, s33
	v_perm_b32 v81, v67, v66, s0
	v_perm_b32 v66, v67, v66, s1
	v_pk_fma_f16 v67, v78, s59, v71 op_sel_hi:[1,0,1]
	v_readlane_b32 s60, v120, 44
	s_waitcnt vmcnt(31)
	v_alignbit_b32 v224, v72, v72, 4
	v_pk_fma_f16 v71, v80, s59, v77 op_sel_hi:[1,0,1]
	v_pk_fma_f16 v77, v81, s59, v79 op_sel_hi:[1,0,1]
	v_pk_fma_f16 v7, v66, s59, v7 op_sel_hi:[1,0,1]
	v_and_b32_e32 v66, 0x7070707, v72
	v_and_b32_e32 v78, 0x7070707, v224
	v_perm_b32 v66, s2, v205, v66
	v_perm_b32 v78, s2, v205, v78
	v_and_or_b32 v66, v72, s4, v66
	v_and_or_b32 v72, v224, s4, v78
	v_perm_b32 v80, v72, v66, s0
	v_perm_b32 v78, v72, v66, s5
	v_perm_b32 v79, v72, v66, s33
	v_perm_b32 v66, v72, v66, s1
	v_pk_fma_f16 v72, v80, s60, v76 op_sel_hi:[1,0,1]
	s_add_u32 s66, s22, s64
	s_addc_u32 s67, s23, s65
	global_load_dwordx2 v[80:81], v121, s[66:67]
	v_alignbit_b32 v225, v73, v73, 4
	v_pk_fma_f16 v8, v66, s60, v8 op_sel_hi:[1,0,1]
	v_and_b32_e32 v66, 0x7070707, v73
	v_and_b32_e32 v76, 0x7070707, v225
	v_pk_fma_f16 v9, v78, s60, v9 op_sel_hi:[1,0,1]
	v_perm_b32 v66, s2, v205, v66
	v_perm_b32 v76, s2, v205, v76
	v_and_or_b32 v66, v73, s4, v66
	v_and_or_b32 v73, v225, s4, v76
	v_perm_b32 v76, v73, v66, s5
	v_pk_fma_f16 v70, v79, s60, v70 op_sel_hi:[1,0,1]
	v_perm_b32 v78, v73, v66, s33
	v_perm_b32 v79, v73, v66, s0
	v_perm_b32 v66, v73, v66, s1
	v_pk_fma_f16 v67, v76, s60, v67 op_sel_hi:[1,0,1]
	v_readlane_b32 s36, v120, 48
	s_waitcnt vmcnt(30)
	v_alignbit_b32 v224, v68, v68, 4
	v_pk_fma_f16 v71, v78, s60, v71 op_sel_hi:[1,0,1]
	v_pk_fma_f16 v73, v79, s60, v77 op_sel_hi:[1,0,1]
	v_pk_fma_f16 v7, v66, s60, v7 op_sel_hi:[1,0,1]
	v_and_b32_e32 v66, 0x7070707, v68
	v_and_b32_e32 v76, 0x7070707, v224
	v_perm_b32 v66, s2, v205, v66
	v_perm_b32 v76, s2, v205, v76
	v_and_or_b32 v66, v68, s4, v66
	v_and_or_b32 v68, v224, s4, v76
	v_perm_b32 v77, v68, v66, s33
	v_perm_b32 v78, v68, v66, s0
	v_perm_b32 v76, v68, v66, s5
	v_perm_b32 v66, v68, v66, s1
	v_pk_fma_f16 v68, v77, s36, v70 op_sel_hi:[1,0,1]
	v_pk_fma_f16 v70, v78, s36, v72 op_sel_hi:[1,0,1]
	s_add_u32 s66, s24, s64
	s_addc_u32 s67, s25, s65
	global_load_dwordx2 v[78:79], v121, s[66:67]
	v_alignbit_b32 v225, v69, v69, 4
	v_pk_fma_f16 v8, v66, s36, v8 op_sel_hi:[1,0,1]
	v_and_b32_e32 v66, 0x7070707, v69
	v_and_b32_e32 v72, 0x7070707, v225
	v_pk_fma_f16 v9, v76, s36, v9 op_sel_hi:[1,0,1]
	v_perm_b32 v66, s2, v205, v66
	v_perm_b32 v72, s2, v205, v72
	v_and_or_b32 v66, v69, s4, v66
	v_and_or_b32 v69, v225, s4, v72
	v_perm_b32 v72, v69, v66, s5
	v_perm_b32 v76, v69, v66, s33
	v_perm_b32 v77, v69, v66, s0
	v_perm_b32 v66, v69, v66, s1
	v_pk_fma_f16 v67, v72, s36, v67 op_sel_hi:[1,0,1]
	v_readlane_b32 s59, v120, 52
	s_waitcnt vmcnt(29)
	v_alignbit_b32 v224, v64, v64, 4
	v_pk_fma_f16 v69, v76, s36, v71 op_sel_hi:[1,0,1]
	v_pk_fma_f16 v71, v77, s36, v73 op_sel_hi:[1,0,1]
	v_pk_fma_f16 v7, v66, s36, v7 op_sel_hi:[1,0,1]
	v_and_b32_e32 v66, 0x7070707, v64
	v_and_b32_e32 v72, 0x7070707, v224
	v_perm_b32 v66, s2, v205, v66
	v_perm_b32 v72, s2, v205, v72
	v_and_or_b32 v66, v64, s4, v66
	v_and_or_b32 v64, v224, s4, v72
	v_perm_b32 v73, v64, v66, s33
	v_perm_b32 v76, v64, v66, s0
	v_perm_b32 v72, v64, v66, s5
	v_perm_b32 v64, v64, v66, s1
	v_pk_fma_f16 v66, v73, s59, v68 op_sel_hi:[1,0,1]
	v_pk_fma_f16 v68, v76, s59, v70 op_sel_hi:[1,0,1]
	s_add_u32 s66, s26, s64
	s_addc_u32 s67, s27, s65
	global_load_dwordx2 v[76:77], v121, s[66:67]
	v_alignbit_b32 v225, v65, v65, 4
	v_pk_fma_f16 v8, v64, s59, v8 op_sel_hi:[1,0,1]
	v_and_b32_e32 v64, 0x7070707, v65
	v_and_b32_e32 v70, 0x7070707, v225
	v_pk_fma_f16 v9, v72, s59, v9 op_sel_hi:[1,0,1]
	v_perm_b32 v64, s2, v205, v64
	v_perm_b32 v70, s2, v205, v70
	v_and_or_b32 v64, v65, s4, v64
	v_and_or_b32 v65, v225, s4, v70
	v_perm_b32 v70, v65, v64, s5
	v_perm_b32 v72, v65, v64, s33
	v_perm_b32 v73, v65, v64, s0
	v_perm_b32 v64, v65, v64, s1
	v_pk_fma_f16 v65, v70, s59, v67 op_sel_hi:[1,0,1]
	v_readlane_b32 s60, v120, 56
	s_waitcnt vmcnt(31)
	v_alignbit_b32 v224, v62, v62, 4
	v_pk_fma_f16 v67, v72, s59, v69 op_sel_hi:[1,0,1]
	v_pk_fma_f16 v69, v73, s59, v71 op_sel_hi:[1,0,1]
	v_pk_fma_f16 v7, v64, s59, v7 op_sel_hi:[1,0,1]
	v_and_b32_e32 v64, 0x7070707, v62
	v_and_b32_e32 v70, 0x7070707, v224
	v_perm_b32 v64, s2, v205, v64
	v_perm_b32 v70, s2, v205, v70
	v_and_or_b32 v64, v62, s4, v64
	v_and_or_b32 v62, v224, s4, v70
	v_perm_b32 v71, v62, v64, s33
	v_perm_b32 v72, v62, v64, s0
	v_perm_b32 v70, v62, v64, s5
	v_perm_b32 v62, v62, v64, s1
	v_pk_fma_f16 v64, v71, s60, v66 op_sel_hi:[1,0,1]
	v_pk_fma_f16 v66, v72, s60, v68 op_sel_hi:[1,0,1]
	s_add_u32 s66, s34, s64
	s_addc_u32 s67, s35, s65
	global_load_dwordx2 v[72:73], v121, s[66:67]
	v_alignbit_b32 v225, v63, v63, 4
	v_pk_fma_f16 v8, v62, s60, v8 op_sel_hi:[1,0,1]
	v_and_b32_e32 v62, 0x7070707, v63
	v_and_b32_e32 v68, 0x7070707, v225
	v_pk_fma_f16 v9, v70, s60, v9 op_sel_hi:[1,0,1]
	v_perm_b32 v62, s2, v205, v62
	v_perm_b32 v68, s2, v205, v68
	v_and_or_b32 v62, v63, s4, v62
	v_and_or_b32 v63, v225, s4, v68
	v_perm_b32 v68, v63, v62, s5
	v_perm_b32 v70, v63, v62, s33
	v_perm_b32 v71, v63, v62, s0
	v_perm_b32 v62, v63, v62, s1
	v_pk_fma_f16 v7, v62, s60, v7 op_sel_hi:[1,0,1]
	v_readlane_b32 s36, v120, 60
	s_waitcnt vmcnt(29)
	v_alignbit_b32 v224, v50, v50, 4
	v_pk_fma_f16 v63, v68, s60, v65 op_sel_hi:[1,0,1]
	v_pk_fma_f16 v65, v70, s60, v67 op_sel_hi:[1,0,1]
	v_pk_fma_f16 v67, v71, s60, v69 op_sel_hi:[1,0,1]
	s_add_u32 s66, s28, s64
	s_addc_u32 s67, s29, s65
	global_load_dwordx2 v[70:71], v121, s[66:67]
	v_and_b32_e32 v15, 0x7070707, v50
	v_and_b32_e32 v62, 0x7070707, v224
	v_perm_b32 v15, s2, v205, v15
	v_perm_b32 v62, s2, v205, v62
	v_and_or_b32 v15, v50, s4, v15
	v_and_or_b32 v50, v224, s4, v62
	v_perm_b32 v62, v50, v15, s5
	v_perm_b32 v68, v50, v15, s33
	v_perm_b32 v69, v50, v15, s0
	v_perm_b32 v15, v50, v15, s1
	v_pk_fma_f16 v105, v62, s36, v9 op_sel_hi:[1,0,1]
	v_alignbit_b32 v225, v51, v51, 4
	v_pk_fma_f16 v102, v15, s36, v8 op_sel_hi:[1,0,1]
	v_and_b32_e32 v8, 0x7070707, v51
	v_and_b32_e32 v9, 0x7070707, v225
	v_perm_b32 v8, s2, v205, v8
	v_perm_b32 v9, s2, v205, v9
	v_and_or_b32 v8, v51, s4, v8
	v_and_or_b32 v9, v225, s4, v9
	v_perm_b32 v15, v9, v8, s5
	v_perm_b32 v50, v9, v8, s33
	v_perm_b32 v51, v9, v8, s0
	v_perm_b32 v8, v9, v8, s1
	v_pk_fma_f16 v104, v68, s36, v64 op_sel_hi:[1,0,1]
	v_pk_fma_f16 v103, v69, s36, v66 op_sel_hi:[1,0,1]
	s_add_u32 s66, s38, s64
	s_addc_u32 s67, s39, s65
	global_load_dwordx2 v[68:69], v121, s[66:67]
	v_pk_fma_f16 v101, v15, s36, v63 op_sel_hi:[1,0,1]
	s_add_u32 s66, s52, s64
	s_addc_u32 s67, s53, s65
	global_load_dwordx2 v[62:63], v121, s[66:67]
	v_pk_fma_f16 v100, v50, s36, v65 op_sel_hi:[1,0,1]
	s_add_u32 s66, s50, s64
	s_addc_u32 s67, s51, s65
	global_load_dwordx2 v[64:65], v121, s[66:67]
	v_pk_fma_f16 v99, v51, s36, v67 op_sel_hi:[1,0,1]
	s_add_u32 s66, s30, s64
	s_addc_u32 s67, s31, s65
	global_load_dwordx2 v[66:67], v121, s[66:67]
	s_add_u32 s66, s54, s64
	s_addc_u32 s67, s55, s65
	global_load_dwordx2 v[50:51], v121, s[66:67]
	v_pk_fma_f16 v15, v8, s36, v7 op_sel_hi:[1,0,1]
	s_cmpk_eq_i32 s56, 0x90
	s_cbranch_scc0 .LBB0_770
	v_lshl_add_u64 v[94:95], v[2:3], 2, v[44:45]
	v_mov_b32_e32 v106, v208
	v_mov_b32_e32 v107, v209
	v_mov_b32_e32 v108, v210
	v_mov_b32_e32 v109, v211
	v_mov_b32_e32 v8, v212
	v_mov_b32_e32 v9, v213
	v_mov_b32_e32 v10, v214
	v_mov_b32_e32 v11, v215
	v_mov_b32_e32 v4, v216
	v_mov_b32_e32 v5, v217
	v_mov_b32_e32 v6, v218
	v_mov_b32_e32 v7, v219
	v_mov_b32_e32 v0, v220
	v_mov_b32_e32 v1, v221
	v_mov_b32_e32 v2, v222
	v_mov_b32_e32 v3, v223
	v_cvt_f32_f16_sdwa v13, v105 dst_sel:DWORD dst_unused:UNUSED_PAD src0_sel:WORD_1
	v_cvt_f32_f16_e32 v12, v105
	s_mov_b32 s12, 0x800000
	v_readlane_b32 s10, v255, 5
	v_readlane_b32 s11, v255, 6
	v_pk_add_f32 v[0:1], v[0:1], v[12:13]
	v_cvt_f32_f16_sdwa v13, v104 dst_sel:DWORD dst_unused:UNUSED_PAD src0_sel:WORD_1
	v_cvt_f32_f16_e32 v12, v104
	v_lshl_add_u64 v[48:49], v[48:49], 0, s[10:11]
	v_pk_add_f32 v[2:3], v[2:3], v[12:13]
	v_cvt_f32_f16_sdwa v13, v103 dst_sel:DWORD dst_unused:UNUSED_PAD src0_sel:WORD_1
	v_cvt_f32_f16_e32 v12, v103
	global_store_dwordx4 v[94:95], v[0:3], off
	v_pk_add_f32 v[4:5], v[4:5], v[12:13]
	v_cvt_f32_f16_sdwa v13, v102 dst_sel:DWORD dst_unused:UNUSED_PAD src0_sel:WORD_1
	v_cvt_f32_f16_e32 v12, v102
	v_mov_b32_e32 v102, v1
	v_mov_b32_e32 v103, v5
	v_pk_mul_f32 v[102:103], v[102:103], v[102:103]
	v_pk_add_f32 v[6:7], v[6:7], v[12:13]
	v_mov_b32_e32 v12, v0
	v_mov_b32_e32 v13, v4
	v_pk_fma_f32 v[12:13], v[12:13], v[12:13], v[102:103]
	v_mov_b32_e32 v102, v2
	v_mov_b32_e32 v103, v6
	v_pk_fma_f32 v[12:13], v[102:103], v[102:103], v[12:13]
	v_mov_b32_e32 v102, v3
	v_mov_b32_e32 v103, v7
	v_pk_fma_f32 v[102:103], v[102:103], v[102:103], v[12:13]
	v_cvt_f32_f16_sdwa v13, v101 dst_sel:DWORD dst_unused:UNUSED_PAD src0_sel:WORD_1
	v_cvt_f32_f16_e32 v12, v101
	v_cvt_f32_f16_sdwa v101, v15 dst_sel:DWORD dst_unused:UNUSED_PAD src0_sel:WORD_1
	global_store_dwordx4 v[94:95], v[4:7], off offset:16
	v_pk_add_f32 v[8:9], v[8:9], v[12:13]
	v_cvt_f32_f16_sdwa v13, v100 dst_sel:DWORD dst_unused:UNUSED_PAD src0_sel:WORD_1
	v_cvt_f32_f16_e32 v12, v100
	v_cvt_f32_f16_e32 v100, v15
	v_pk_add_f32 v[10:11], v[10:11], v[12:13]
	v_cvt_f32_f16_sdwa v13, v99 dst_sel:DWORD dst_unused:UNUSED_PAD src0_sel:WORD_1
	v_cvt_f32_f16_e32 v12, v99
	v_pk_add_f32 v[14:15], v[108:109], v[100:101]
	v_mov_b32_e32 v100, v9
	global_store_dwordx4 v[94:95], v[8:11], off offset:32
	v_pk_add_f32 v[12:13], v[106:107], v[12:13]
	global_store_dwordx4 v[94:95], v[12:15], off offset:48
	v_mov_b32_e32 v101, v13
	v_mov_b32_e32 v94, v8
	v_mov_b32_e32 v95, v12
	v_pk_mul_f32 v[100:101], v[100:101], v[100:101]
	v_add_f32_e32 v99, v102, v103
	v_pk_fma_f32 v[94:95], v[94:95], v[94:95], v[100:101]
	v_mov_b32_e32 v100, v10
	v_mov_b32_e32 v101, v14
	v_pk_fma_f32 v[94:95], v[100:101], v[100:101], v[94:95]
	v_mov_b32_e32 v100, v11
	v_mov_b32_e32 v101, v15
	v_pk_fma_f32 v[94:95], v[100:101], v[100:101], v[94:95]
	global_load_dwordx4 v[100:103], v[46:47], off offset:48
	global_load_dwordx4 v[104:107], v[46:47], off offset:32
	global_load_dwordx4 v[108:111], v[46:47], off offset:16
	global_load_dwordx4 v[112:115], v[46:47], off
	v_add_f32_e32 v94, v99, v94
	v_add_f32_e32 v94, v94, v95
	v_mov_b32_e32 v95, v94
	s_nop 1
	v_permlane32_swap_b32 v95, v94
	s_waitcnt lgkmcnt(0)
	v_add_f32_e32 v94, v94, v95
	v_mov_b32_e32 v95, v94
	s_nop 1
	v_permlane16_swap_b32 v95, v94
	s_waitcnt lgkmcnt(0)
	v_add_f32_e32 v94, v94, v95
	s_nop 1
	v_mov_b32_dpp v95, v94 row_ror:8 row_mask:0xf bank_mask:0xf
	s_waitcnt lgkmcnt(0)
	v_add_f32_e32 v94, v94, v95
	s_nop 1
	v_mov_b32_dpp v95, v94 row_half_mirror row_mask:0xf bank_mask:0xf
	s_nop 1
	v_mov_b32_dpp v95, v95 quad_perm:[3,2,1,0] row_mask:0xf bank_mask:0xf
	s_waitcnt lgkmcnt(0)
	v_add_f32_e32 v94, v94, v95
	s_nop 1
	v_mov_b32_dpp v95, v94 quad_perm:[2,3,0,1] row_mask:0xf bank_mask:0xf
	s_waitcnt lgkmcnt(0)
	v_add_f32_e32 v94, v94, v95
	s_nop 1
	v_mov_b32_dpp v95, v94 quad_perm:[1,0,3,2] row_mask:0xf bank_mask:0xf
	s_waitcnt lgkmcnt(0)
	v_add_f32_e32 v94, v94, v95
	v_fmamk_f32 v94, v94, 0x3a800000, v191
	v_cmp_gt_f32_e32 vcc, s12, v94
	v_mul_f32_e32 v95, 0x4b800000, v94
	s_nop 0
	v_cndmask_b32_e32 v94, v94, v95, vcc
	v_rsq_f32_e32 v94, v94
	s_nop 0
	v_mul_f32_e32 v95, 0x45800000, v94
	v_cndmask_b32_e32 v94, v94, v95, vcc
	v_pk_mul_f32 v[0:1], v[0:1], v[94:95] op_sel_hi:[1,0]
	v_pk_mul_f32 v[2:3], v[2:3], v[94:95] op_sel_hi:[1,0]
	s_waitcnt vmcnt(0)
	v_pk_mul_f32 v[0:1], v[112:113], v[0:1]
	v_pk_mul_f32 v[2:3], v[114:115], v[2:3]
	v_cvt_pk_bf16_f32 v0, v0, v1
	v_cvt_pk_bf16_f32 v1, v2, v3
	v_pk_mul_f32 v[2:3], v[4:5], v[94:95] op_sel_hi:[1,0]
	v_pk_mul_f32 v[4:5], v[6:7], v[94:95] op_sel_hi:[1,0]
	v_pk_mul_f32 v[2:3], v[108:109], v[2:3]
	v_pk_mul_f32 v[4:5], v[110:111], v[4:5]
	v_cvt_pk_bf16_f32 v2, v2, v3
	v_cvt_pk_bf16_f32 v3, v4, v5
	v_pk_mul_f32 v[4:5], v[8:9], v[94:95] op_sel_hi:[1,0]
	v_pk_mul_f32 v[6:7], v[10:11], v[94:95] op_sel_hi:[1,0]
	v_pk_mul_f32 v[4:5], v[104:105], v[4:5]
	v_pk_mul_f32 v[6:7], v[6:7], v[106:107]
	v_cvt_pk_bf16_f32 v4, v4, v5
	v_cvt_pk_bf16_f32 v5, v6, v7
	v_pk_mul_f32 v[6:7], v[12:13], v[94:95] op_sel_hi:[1,0]
	v_pk_mul_f32 v[8:9], v[14:15], v[94:95] op_sel_hi:[1,0]
	v_pk_mul_f32 v[6:7], v[6:7], v[100:101]
	v_pk_mul_f32 v[8:9], v[8:9], v[102:103]
	v_cvt_pk_bf16_f32 v6, v6, v7
	v_cvt_pk_bf16_f32 v7, v8, v9
	global_store_dwordx4 v[74:75], v[0:3], off
	global_store_dwordx4 v[74:75], v[4:7], off offset:16
	s_nop 0
	v_mov_b32_e32 v0, v98
	s_andn2_b64 exec, exec, s[8:9]
	s_cbranch_execnz .LBB0_769
